# attention softmax max/sum exchanges via v_permlane16/32_swap; retention core: redundant barrier B1 removed
# baseline (speedup 1.0000x reference)
; #define LAS __attribute__((address_space(3)))
; template <int VAR  >
; __device__ __forceinline__ void ret_core_mfma(const bf16* P, const bf16* VT, const float* decay_logit  , bf16* YF, bf16* YB, float* PT, LAS unsigned char* lds, const int tid, const int bid, const int G) {
;     ...
;             for (int n = 0; n < 16; ++n) acc4[n] = acc4[n] * cdec;
;             const int jj = 8 * fqc + (frc >> 2);
;             const unsigned trA = (unsigned)((jj >> 4) * 1024 + sl_swz((jj & 15) * 64 + 8 * (frc & 3))), trB = (unsigned)(((jj + 4) >> 4) * 1024 + sl_swz(((jj + 4) & 15) * 64 + 8 * (frc & 3)));
;             f32x4 accA[4][2], accY[4][2];
; #pragma unroll
;             for (int m = 0; m < 4; ++m)
; #pragma unroll
;                 for (int n = 0; n < 2; ++n) { accA[m][n] = (f32x4){0.f, 0.f, 0.f, 0.f}; accY[m][n] = (f32x4){0.f, 0.f, 0.f, 0.f}; }
; #pragma unroll
;             for (int ks = 0; ks < 8; ++ks) {
;                 if (ks < 4) { if (c == 0) RC_WAITV(6); else RC_WAITV(14); } else if (ks == 4) RC_WAITV(6); else if (ks == 5) RC_WAITV(5); else if (ks == 6) RC_WAITV(4); else RC_WAITV(3);
;                 RC_BAR();
;                 { const int s4 = RC_PREV(slot);
;                   if (ks + 4 < 12) RC_ISSUE(ks + 4, tok0, s4); else RC_ISSUE(ks + 4 - 12, tokn, s4); }
;                 bf16x8v At[4], Bk[2], Bs[2];
;                 const LAS unsigned char* sq = lds + RC_RG + slot * 16384;
; #pragma unroll
;                 for (int m = 0; m < 4; ++m) At[m] = *(const LAS bf16x8v*)(sq + aoff + m * 1024);
; #pragma unroll
;                 for (int n = 0; n < 2; ++n) { Bk[n] = *(const LAS bf16x8v*)(sq + 8192 + boff + n * 1024); Bs[n] = *(const LAS bf16x8v*)(lds + RC_ST + ks * 8192 + boff + n * 1024); }
; #pragma unroll
;                 for (int m = 0; m < 4; ++m)
; #pragma unroll
;                     for (int n = 0; n < 2; ++n) { accA[m][n] = RC_MFMA(Bk[n], At[m], accA[m][n]); accY[m][n] = RC_MFMA(Bs[n], At[m], accY[m][n]); }
;                 { const unsigned kb = (unsigned)(size_t)(sq + 8192);
;                   const unsigned a0 = kb + trA, a1 = kb + trB, b0 = kb + (trA ^ 32u), b1 = kb + (trB ^ 32u);
;                   v2u l0, h0, l1, h1, l2, h2, l3, h3, p0, q0, p1, q1, p2, q2, p3, q3;
;                   asm volatile("ds_read_b64_tr_b16 %0, %16\n\tds_read_b64_tr_b16 %1, %17\n\tds_read_b64_tr_b16 %8, %18\n\tds_read_b64_tr_b16 %9, %19\n\t"
.LBB0_55:
	s_add_i32 s0, s40, 1
	s_cmp_lg_u32 s40, 4
	s_cselect_b32 s0, s0, 0
	s_lshl_b32 s60, s38, 7
	s_add_i32 s6, s33, 1
	s_cmp_eq_u32 s33, 15
	s_cselect_b32 s1, 0, s39
	s_cselect_b32 s7, 15, s6
	s_and_b64 s[40:41], s[4:5], exec
	s_cselect_b32 s7, s7, s1
	s_lshl_b32 s1, s0, 14
	s_lshl_b32 s40, s38, 8
	s_add_i32 s33, s1, 0xffffc000
	s_cmp_lg_u32 s0, 0
	s_cselect_b32 s33, s33, 0x10000
	s_mov_b32 s41, s61
	s_add_i32 s33, s33, 0
	v_lshl_add_u64 v[148:149], v[220:221], 0, s[40:41]
	s_mov_b64 s[40:41], 0x1c0
	s_add_i32 s33, s33, s44
	s_barrier
	v_lshl_add_u64 v[150:151], v[232:233], 0, s[40:41]
	s_add_i32 m0, s33, 0x10000
	s_mov_b64 s[40:41], 0x9c0
	global_load_lds_dwordx4 v[150:151], off
	v_lshl_add_u64 v[150:151], v[232:233], 0, s[40:41]
	s_add_i32 m0, s33, 0x12000
	s_add_i32 s1, s86, s1
	global_load_lds_dwordx4 v[150:151], off
	v_add_u32_e32 v170, s1, v242
	v_add_u32_e32 v178, s1, v243
	ds_read_b128 v[150:153], v236 offset:25600
	ds_read_b128 v[154:157], v236 offset:24576
	ds_read_b128 v[158:161], v170
	ds_read_b128 v[162:165], v170 offset:1024
	ds_read_b128 v[166:169], v170 offset:2048
	ds_read_b128 v[170:173], v170 offset:3072
	ds_read_b128 v[174:177], v178 offset:8192
	ds_read_b128 v[178:181], v178 offset:9216
	v_mov_b32_e32 v217, v216
	v_pk_mul_f32 v[26:27], v[216:217], v[26:27]
	v_pk_mul_f32 v[24:25], v[224:225], v[24:25]
	v_pk_mul_f32 v[22:23], v[216:217], v[22:23]
	v_pk_mul_f32 v[20:21], v[224:225], v[20:21]
	s_add_i32 s33, s1, 0x2000
	s_waitcnt lgkmcnt(0)
	v_mfma_f32_16x16x32_bf16 v[96:99], v[174:177], v[158:161], v[96:99]
	v_add_u32_e32 v182, s33, v234
	v_add_u32_e32 v183, s33, v231
	v_add_u32_e32 v184, s33, v227
	v_mfma_f32_16x16x32_bf16 v[100:103], v[154:157], v[158:161], v[100:103]
	v_add_u32_e32 v185, s33, v229
	s_add_i32 s1, s0, 1
	s_cmp_lg_u32 s0, 4
	v_mfma_f32_16x16x32_bf16 v[104:107], v[178:181], v[158:161], v[104:107]
	s_cselect_b32 s0, s1, 0
	s_lshl_b32 s1, s0, 14
	s_add_i32 s33, s1, 0xffffc000
	v_mfma_f32_16x16x32_bf16 v[108:111], v[150:153], v[158:161], v[108:111]
	s_cmp_lg_u32 s0, 0
	s_cselect_b32 s33, s33, 0x10000
	s_add_i32 s33, s33, 0
	v_mfma_f32_16x16x32_bf16 v[112:115], v[174:177], v[162:165], v[112:115]
	s_add_i32 s33, s33, s44
	s_add_i32 m0, s33, 0x10000
	s_add_i32 s1, s86, s1
	v_mfma_f32_16x16x32_bf16 v[116:119], v[154:157], v[162:165], v[116:119]
	v_mul_f32_e64 v30, v216, v30
	v_mul_f32_e64 v31, v217, v31
	v_pk_mul_f32 v[28:29], v[224:225], v[28:29]
	s_add_i32 s33, s1, 0x2000
	v_mfma_f32_16x16x32_bf16 v[120:123], v[178:181], v[162:165], v[120:123]
	v_mul_f32_e64 v34, v216, v34
	v_mul_f32_e64 v35, v217, v35
	v_pk_mul_f32 v[32:33], v[224:225], v[32:33]
	v_pk_mul_f32 v[46:47], v[216:217], v[46:47]
	v_mfma_f32_16x16x32_bf16 v[124:127], v[150:153], v[162:165], v[124:127]
	v_mul_f32_e64 v44, v224, v44
	v_mul_f32_e64 v45, v225, v45
	v_pk_mul_f32 v[50:51], v[216:217], v[50:51]
	v_pk_mul_f32 v[48:49], v[224:225], v[48:49]
	v_mfma_f32_16x16x32_bf16 v[128:131], v[174:177], v[166:169], v[128:131]
	v_mul_f32_e64 v58, v216, v58
	v_mul_f32_e64 v59, v217, v59
	v_pk_mul_f32 v[56:57], v[224:225], v[56:57]
	v_pk_mul_f32 v[54:55], v[216:217], v[54:55]
	v_mfma_f32_16x16x32_bf16 v[132:135], v[154:157], v[166:169], v[132:135]
	v_mul_f32_e64 v52, v224, v52
	v_mul_f32_e64 v53, v225, v53
	v_pk_mul_f32 v[62:63], v[216:217], v[62:63]
	v_pk_mul_f32 v[60:61], v[224:225], v[60:61]
	v_mfma_f32_16x16x32_bf16 v[136:139], v[178:181], v[166:169], v[136:139]
	v_mul_f32_e64 v66, v216, v66
	v_mul_f32_e64 v67, v217, v67
	v_pk_mul_f32 v[64:65], v[224:225], v[64:65]
	v_and_b32_e32 v2, 15, v230
	v_mfma_f32_16x16x32_bf16 v[140:143], v[150:153], v[166:169], v[140:143]
	v_mfma_f32_16x16x32_bf16 v[144:147], v[174:177], v[170:173], v[144:147]
	v_mfma_f32_16x16x32_bf16 v[88:91], v[154:157], v[170:173], v[88:91]
	v_mfma_f32_16x16x32_bf16 v[84:87], v[178:181], v[170:173], v[84:87]
	v_mfma_f32_16x16x32_bf16 v[92:95], v[150:153], v[170:173], v[92:95]
	ds_read_b64_tr_b16 v[178:179], v182
	ds_read_b64_tr_b16 v[180:181], v183
	ds_read_b64_tr_b16 v[174:175], v184
	ds_read_b64_tr_b16 v[176:177], v185
	ds_read_b64_tr_b16 v[170:171], v182 offset:2048
	ds_read_b64_tr_b16 v[172:173], v183 offset:2048
	ds_read_b64_tr_b16 v[166:167], v184 offset:2048
	ds_read_b64_tr_b16 v[168:169], v185 offset:2048
	ds_read_b64_tr_b16 v[162:163], v182 offset:4096
	ds_read_b64_tr_b16 v[164:165], v183 offset:4096
	ds_read_b64_tr_b16 v[158:159], v184 offset:4096
	ds_read_b64_tr_b16 v[160:161], v185 offset:4096
	ds_read_b64_tr_b16 v[154:155], v182 offset:6144
	ds_read_b64_tr_b16 v[156:157], v183 offset:6144
	ds_read_b64_tr_b16 v[150:151], v184 offset:6144
	ds_read_b64_tr_b16 v[152:153], v185 offset:6144
	s_waitcnt lgkmcnt(0)
	s_waitcnt vmcnt(6)
	s_barrier
; template <int VAR  >
; __device__ __forceinline__ void ret_core_mfma(const bf16* P, const bf16* VT, const float* decay_logit  , bf16* YF, bf16* YB, float* PT, LAS unsigned char* lds, const int tid, const int bid, const int G) {
;     ...
;             for (int ks = 0; ks < 8; ++ks) {
;                 if (ks < 4) { if (c == 0) RC_WAITV(6); else RC_WAITV(14); } else if (ks == 4) RC_WAITV(6); else if (ks == 5) RC_WAITV(5); else if (ks == 6) RC_WAITV(4); else RC_WAITV(3);
;                 RC_BAR();
;                 { const int s4 = RC_PREV(slot);
;                   if (ks + 4 < 12) RC_ISSUE(ks + 4, tok0, s4); else RC_ISSUE(ks + 4 - 12, tokn, s4); }
;                 bf16x8v At[4], Bk[2], Bs[2];
;                 const LAS unsigned char* sq = lds + RC_RG + slot * 16384;
; #pragma unroll
;                 for (int m = 0; m < 4; ++m) At[m] = *(const LAS bf16x8v*)(sq + aoff + m * 1024);
; #pragma unroll
;                 for (int n = 0; n < 2; ++n) { Bk[n] = *(const LAS bf16x8v*)(sq + 8192 + boff + n * 1024); Bs[n] = *(const LAS bf16x8v*)(lds + RC_ST + ks * 8192 + boff + n * 1024); }
; #pragma unroll
;                 for (int m = 0; m < 4; ++m)
; #pragma unroll
;                     for (int n = 0; n < 2; ++n) { accA[m][n] = RC_MFMA(Bk[n], At[m], accA[m][n]); accY[m][n] = RC_MFMA(Bs[n], At[m], accY[m][n]); }
;                 { const unsigned kb = (unsigned)(size_t)(sq + 8192);
;                   const unsigned a0 = kb + trA, a1 = kb + trB, b0 = kb + (trA ^ 32u), b1 = kb + (trB ^ 32u);
;                   v2u l0, h0, l1, h1, l2, h2, l3, h3, p0, q0, p1, q1, p2, q2, p3, q3;
;                   asm volatile("ds_read_b64_tr_b16 %0, %16\n\tds_read_b64_tr_b16 %1, %17\n\tds_read_b64_tr_b16 %8, %18\n\tds_read_b64_tr_b16 %9, %19\n\t"
;                                "ds_read_b64_tr_b16 %2, %16 offset:2048\n\tds_read_b64_tr_b16 %3, %17 offset:2048\n\tds_read_b64_tr_b16 %10, %18 offset:2048\n\tds_read_b64_tr_b16 %11, %19 offset:2048\n\t"
;                                "ds_read_b64_tr_b16 %4, %16 offset:4096\n\tds_read_b64_tr_b16 %5, %17 offset:4096\n\tds_read_b64_tr_b16 %12, %18 offset:4096\n\tds_read_b64_tr_b16 %13, %19 offset:4096\n\t"
;                                "ds_read_b64_tr_b16 %6, %16 offset:6144\n\tds_read_b64_tr_b16 %7, %17 offset:6144\n\tds_read_b64_tr_b16 %14, %18 offset:6144\n\tds_read_b64_tr_b16 %15, %19 offset:6144\n\ts_waitcnt lgkmcnt(0)"
	v_mfma_f32_16x16x32_bf16 v[24:27], v[178:181], v[68:71], v[24:27]
	global_load_lds_dwordx4 v[148:149], off
	v_mfma_f32_16x16x32_bf16 v[20:23], v[174:177], v[68:71], v[20:23]
	v_add_u32_e32 v178, s1, v243
	v_mfma_f32_16x16x32_bf16 v[24:27], v[170:173], v[72:75], v[24:27]
	v_add_u32_e32 v170, s1, v242
	s_add_i32 s1, s0, 1
	s_cmp_lg_u32 s0, 4
	v_mfma_f32_16x16x32_bf16 v[20:23], v[166:169], v[72:75], v[20:23]
	s_cselect_b32 s0, s1, 0
	s_lshl_b32 s1, s0, 14
	v_mfma_f32_16x16x32_bf16 v[24:27], v[162:165], v[76:79], v[24:27]
	v_mfma_f32_16x16x32_bf16 v[20:23], v[158:161], v[76:79], v[20:23]
	v_mfma_f32_16x16x32_bf16 v[24:27], v[154:157], v[80:83], v[24:27]
	v_mfma_f32_16x16x32_bf16 v[20:23], v[150:153], v[80:83], v[20:23]
	ds_read_b128 v[150:153], v236 offset:33792
	ds_read_b128 v[154:157], v236 offset:32768
	ds_read_b128 v[158:161], v170
	ds_read_b128 v[162:165], v170 offset:1024
	ds_read_b128 v[166:169], v170 offset:2048
	ds_read_b128 v[170:173], v170 offset:3072
	ds_read_b128 v[174:177], v178 offset:8192
	ds_read_b128 v[178:181], v178 offset:9216
	s_waitcnt lgkmcnt(0)
	v_mfma_f32_16x16x32_bf16 v[96:99], v[174:177], v[158:161], v[96:99]
	v_mfma_f32_16x16x32_bf16 v[100:103], v[154:157], v[158:161], v[100:103]
	v_mfma_f32_16x16x32_bf16 v[104:107], v[178:181], v[158:161], v[104:107]
	v_mfma_f32_16x16x32_bf16 v[108:111], v[150:153], v[158:161], v[108:111]
	v_mfma_f32_16x16x32_bf16 v[112:115], v[174:177], v[162:165], v[112:115]
	v_mfma_f32_16x16x32_bf16 v[158:161], v[154:157], v[162:165], v[116:119]
	v_mfma_f32_16x16x32_bf16 v[182:185], v[178:181], v[162:165], v[120:123]
	v_mfma_f32_16x16x32_bf16 v[162:165], v[150:153], v[162:165], v[124:127]
	v_mfma_f32_16x16x32_bf16 v[186:189], v[174:177], v[166:169], v[128:131]
	v_mfma_f32_16x16x32_bf16 v[132:135], v[154:157], v[166:169], v[132:135]
	v_mfma_f32_16x16x32_bf16 v[120:123], v[178:181], v[166:169], v[136:139]
	v_mfma_f32_16x16x32_bf16 v[124:127], v[150:153], v[166:169], v[140:143]
	v_mfma_f32_16x16x32_bf16 v[128:131], v[174:177], v[170:173], v[144:147]
	v_add_u32_e32 v174, s33, v234
	v_add_u32_e32 v175, s33, v231
	v_add_u32_e32 v176, s33, v227
	v_mfma_f32_16x16x32_bf16 v[136:139], v[154:157], v[170:173], v[88:91]
	v_add_u32_e32 v177, s33, v229
	s_add_i32 s33, s1, 0xffffc000
	s_cmp_lg_u32 s0, 0
	v_mfma_f32_16x16x32_bf16 v[140:143], v[178:181], v[170:173], v[84:87]
	s_cselect_b32 s33, s33, 0x10000
	s_add_i32 s33, s33, 0
	s_add_i32 s33, s33, s44
	v_mfma_f32_16x16x32_bf16 v[150:153], v[150:153], v[170:173], v[92:95]
	ds_read_b64_tr_b16 v[170:171], v174
	ds_read_b64_tr_b16 v[172:173], v175
	ds_read_b64_tr_b16 v[166:167], v176
	ds_read_b64_tr_b16 v[168:169], v177
	ds_read_b64_tr_b16 v[154:155], v174 offset:2048
	ds_read_b64_tr_b16 v[156:157], v175 offset:2048
	ds_read_b64_tr_b16 v[144:145], v176 offset:2048
	ds_read_b64_tr_b16 v[146:147], v177 offset:2048
	ds_read_b64_tr_b16 v[116:117], v174 offset:4096
	ds_read_b64_tr_b16 v[118:119], v175 offset:4096
	ds_read_b64_tr_b16 v[92:93], v176 offset:4096
	ds_read_b64_tr_b16 v[94:95], v177 offset:4096
	ds_read_b64_tr_b16 v[88:89], v174 offset:6144
	ds_read_b64_tr_b16 v[90:91], v175 offset:6144
	ds_read_b64_tr_b16 v[84:85], v176 offset:6144
	ds_read_b64_tr_b16 v[86:87], v177 offset:6144
	s_waitcnt lgkmcnt(0)
	s_waitcnt vmcnt(5)
	s_barrier
	v_mfma_f32_16x16x32_bf16 v[28:31], v[166:169], v[68:71], v[28:31]
	s_add_i32 m0, s33, 0x10000
	s_add_i32 s1, s86, s1
	v_mfma_f32_16x16x32_bf16 v[32:35], v[170:173], v[68:71], v[32:35]
	s_add_i32 s33, s1, 0x2000
	v_mfma_f32_16x16x32_bf16 v[28:31], v[144:147], v[72:75], v[28:31]
	v_mfma_f32_16x16x32_bf16 v[32:35], v[154:157], v[72:75], v[32:35]
	v_mfma_f32_16x16x32_bf16 v[28:31], v[92:95], v[76:79], v[28:31]
	v_mfma_f32_16x16x32_bf16 v[32:35], v[116:119], v[76:79], v[32:35]
	v_mfma_f32_16x16x32_bf16 v[28:31], v[84:87], v[80:83], v[28:31]
	v_lshl_add_u64 v[84:85], v[148:149], 0, 64
	global_load_lds_dwordx4 v[84:85], off
	v_mfma_f32_16x16x32_bf16 v[32:35], v[88:91], v[80:83], v[32:35]
	v_add_u32_e32 v88, s1, v242
	ds_read_b128 v[154:157], v236 offset:41984
	ds_read_b128 v[166:169], v236 offset:40960
	ds_read_b128 v[84:87], v88
	ds_read_b128 v[170:173], v88 offset:1024
	ds_read_b128 v[174:177], v88 offset:2048
	ds_read_b128 v[178:181], v88 offset:3072
	v_add_u32_e32 v88, s1, v243
	ds_read_b128 v[190:193], v88 offset:8192
	ds_read_b128 v[194:197], v88 offset:9216
	s_waitcnt lgkmcnt(0)
	v_mfma_f32_16x16x32_bf16 v[144:147], v[190:193], v[84:87], v[96:99]
	s_add_i32 s1, s0, 1
	s_cmp_lg_u32 s0, 4
	s_cselect_b32 s0, s1, 0
	v_mfma_f32_16x16x32_bf16 v[116:119], v[166:169], v[84:87], v[100:103]
	s_lshl_b32 s1, s0, 14
	v_mfma_f32_16x16x32_bf16 v[104:107], v[194:197], v[84:87], v[104:107]
	v_mfma_f32_16x16x32_bf16 v[84:87], v[154:157], v[84:87], v[108:111]
	v_mfma_f32_16x16x32_bf16 v[88:91], v[190:193], v[170:173], v[112:115]
	v_mfma_f32_16x16x32_bf16 v[92:95], v[166:169], v[170:173], v[158:161]
	v_mfma_f32_16x16x32_bf16 v[96:99], v[194:197], v[170:173], v[182:185]
	v_mfma_f32_16x16x32_bf16 v[100:103], v[154:157], v[170:173], v[162:165]
	s_nop 1
	v_add_u32_e32 v182, s33, v234
	v_add_u32_e32 v183, s33, v231
	v_add_u32_e32 v184, s33, v227
	v_mfma_f32_16x16x32_bf16 v[108:111], v[190:193], v[174:177], v[186:189]
	v_add_u32_e32 v185, s33, v229
	s_add_i32 s33, s1, 0xffffc000
	s_cmp_lg_u32 s0, 0
	v_mfma_f32_16x16x32_bf16 v[112:115], v[166:169], v[174:177], v[132:135]
	s_cselect_b32 s33, s33, 0x10000
	s_add_i32 s33, s33, 0
	s_add_i32 s33, s33, s44
	v_mfma_f32_16x16x32_bf16 v[120:123], v[194:197], v[174:177], v[120:123]
	s_add_i32 m0, s33, 0x10000
	s_add_i32 s1, s86, s1
	s_add_i32 s33, s1, 0x2000
	v_mfma_f32_16x16x32_bf16 v[124:127], v[154:157], v[174:177], v[124:127]
	v_mfma_f32_16x16x32_bf16 v[128:131], v[190:193], v[178:181], v[128:131]
	v_mfma_f32_16x16x32_bf16 v[132:135], v[166:169], v[178:181], v[136:139]
	v_mfma_f32_16x16x32_bf16 v[136:139], v[194:197], v[178:181], v[140:143]
	v_mfma_f32_16x16x32_bf16 v[140:143], v[154:157], v[178:181], v[150:153]
	ds_read_b64_tr_b16 v[178:179], v182
	ds_read_b64_tr_b16 v[180:181], v183
	ds_read_b64_tr_b16 v[174:175], v184
	ds_read_b64_tr_b16 v[176:177], v185
	ds_read_b64_tr_b16 v[170:171], v182 offset:2048
	ds_read_b64_tr_b16 v[172:173], v183 offset:2048
	ds_read_b64_tr_b16 v[166:167], v184 offset:2048
	ds_read_b64_tr_b16 v[168:169], v185 offset:2048
	ds_read_b64_tr_b16 v[162:163], v182 offset:4096
	ds_read_b64_tr_b16 v[164:165], v183 offset:4096
	ds_read_b64_tr_b16 v[158:159], v184 offset:4096
	ds_read_b64_tr_b16 v[160:161], v185 offset:4096
	ds_read_b64_tr_b16 v[154:155], v182 offset:6144
	ds_read_b64_tr_b16 v[156:157], v183 offset:6144
	ds_read_b64_tr_b16 v[150:151], v184 offset:6144
	ds_read_b64_tr_b16 v[152:153], v185 offset:6144
	s_waitcnt lgkmcnt(0)
	s_waitcnt vmcnt(4)
	s_barrier
; template <int VAR  >
; __device__ __forceinline__ void ret_core_mfma(const bf16* P, const bf16* VT, const float* decay_logit  , bf16* YF, bf16* YB, float* PT, LAS unsigned char* lds, const int tid, const int bid, const int G) {
;     ...
;             for (int ks = 0; ks < 8; ++ks) {
;                 if (ks < 4) { if (c == 0) RC_WAITV(6); else RC_WAITV(14); } else if (ks == 4) RC_WAITV(6); else if (ks == 5) RC_WAITV(5); else if (ks == 6) RC_WAITV(4); else RC_WAITV(3);
;                 RC_BAR();
;                 { const int s4 = RC_PREV(slot);
;                   if (ks + 4 < 12) RC_ISSUE(ks + 4, tok0, s4); else RC_ISSUE(ks + 4 - 12, tokn, s4); }
;                 bf16x8v At[4], Bk[2], Bs[2];
;                 const LAS unsigned char* sq = lds + RC_RG + slot * 16384;
; #pragma unroll
;                 for (int m = 0; m < 4; ++m) At[m] = *(const LAS bf16x8v*)(sq + aoff + m * 1024);
; #pragma unroll
;                 for (int n = 0; n < 2; ++n) { Bk[n] = *(const LAS bf16x8v*)(sq + 8192 + boff + n * 1024); Bs[n] = *(const LAS bf16x8v*)(lds + RC_ST + ks * 8192 + boff + n * 1024); }
; #pragma unroll
;                 for (int m = 0; m < 4; ++m)
; #pragma unroll
;                     for (int n = 0; n < 2; ++n) { accA[m][n] = RC_MFMA(Bk[n], At[m], accA[m][n]); accY[m][n] = RC_MFMA(Bs[n], At[m], accY[m][n]); }
;                 { const unsigned kb = (unsigned)(size_t)(sq + 8192);
;                   const unsigned a0 = kb + trA, a1 = kb + trB, b0 = kb + (trA ^ 32u), b1 = kb + (trB ^ 32u);
;                   v2u l0, h0, l1, h1, l2, h2, l3, h3, p0, q0, p1, q1, p2, q2, p3, q3;
;                   asm volatile("ds_read_b64_tr_b16 %0, %16\n\tds_read_b64_tr_b16 %1, %17\n\tds_read_b64_tr_b16 %8, %18\n\tds_read_b64_tr_b16 %9, %19\n\t"
;                                "ds_read_b64_tr_b16 %2, %16 offset:2048\n\tds_read_b64_tr_b16 %3, %17 offset:2048\n\tds_read_b64_tr_b16 %10, %18 offset:2048\n\tds_read_b64_tr_b16 %11, %19 offset:2048\n\t"
;                                "ds_read_b64_tr_b16 %4, %16 offset:4096\n\tds_read_b64_tr_b16 %5, %17 offset:4096\n\tds_read_b64_tr_b16 %12, %18 offset:4096\n\tds_read_b64_tr_b16 %13, %19 offset:4096\n\t"
;                                "ds_read_b64_tr_b16 %6, %16 offset:6144\n\tds_read_b64_tr_b16 %7, %17 offset:6144\n\tds_read_b64_tr_b16 %14, %18 offset:6144\n\tds_read_b64_tr_b16 %15, %19 offset:6144\n\ts_waitcnt lgkmcnt(0)"
	v_mfma_f32_16x16x32_bf16 v[44:47], v[174:177], v[68:71], v[44:47]
	v_mfma_f32_16x16x32_bf16 v[48:51], v[178:181], v[68:71], v[48:51]
	v_add_u32_e32 v178, s1, v243
	v_mfma_f32_16x16x32_bf16 v[44:47], v[166:169], v[72:75], v[44:47]
	v_mfma_f32_16x16x32_bf16 v[48:51], v[170:173], v[72:75], v[48:51]
	v_add_u32_e32 v170, s1, v242
	s_add_i32 s1, s0, 1
	s_cmp_lg_u32 s0, 4
	v_mfma_f32_16x16x32_bf16 v[44:47], v[158:161], v[76:79], v[44:47]
	v_mfma_f32_16x16x32_bf16 v[48:51], v[162:165], v[76:79], v[48:51]
	v_mfma_f32_16x16x32_bf16 v[44:47], v[150:153], v[80:83], v[44:47]
	v_lshl_add_u64 v[150:151], v[148:149], 0, s[66:67]
	global_load_lds_dwordx4 v[150:151], off
	v_mfma_f32_16x16x32_bf16 v[48:51], v[154:157], v[80:83], v[48:51]
	ds_read_b128 v[150:153], v236 offset:50176
	ds_read_b128 v[154:157], v236 offset:49152
	ds_read_b128 v[158:161], v170
	ds_read_b128 v[162:165], v170 offset:1024
	ds_read_b128 v[166:169], v170 offset:2048
	ds_read_b128 v[170:173], v170 offset:3072
	ds_read_b128 v[174:177], v178 offset:8192
	ds_read_b128 v[178:181], v178 offset:9216
	s_waitcnt lgkmcnt(0)
	v_mfma_f32_16x16x32_bf16 v[144:147], v[174:177], v[158:161], v[144:147]
	v_mfma_f32_16x16x32_bf16 v[116:119], v[154:157], v[158:161], v[116:119]
	v_mfma_f32_16x16x32_bf16 v[104:107], v[178:181], v[158:161], v[104:107]
	v_mfma_f32_16x16x32_bf16 v[84:87], v[150:153], v[158:161], v[84:87]
	v_mfma_f32_16x16x32_bf16 v[88:91], v[174:177], v[162:165], v[88:91]
	v_mfma_f32_16x16x32_bf16 v[92:95], v[154:157], v[162:165], v[92:95]
	v_mfma_f32_16x16x32_bf16 v[96:99], v[178:181], v[162:165], v[96:99]
	v_mfma_f32_16x16x32_bf16 v[158:161], v[150:153], v[162:165], v[100:103]
	v_mfma_f32_16x16x32_bf16 v[108:111], v[174:177], v[166:169], v[108:111]
	v_mfma_f32_16x16x32_bf16 v[162:165], v[154:157], v[166:169], v[112:115]
	v_mfma_f32_16x16x32_bf16 v[182:185], v[178:181], v[166:169], v[120:123]
	v_mfma_f32_16x16x32_bf16 v[166:169], v[150:153], v[166:169], v[124:127]
	v_mfma_f32_16x16x32_bf16 v[174:177], v[174:177], v[170:173], v[128:131]
	v_mfma_f32_16x16x32_bf16 v[154:157], v[154:157], v[170:173], v[132:135]
	v_mfma_f32_16x16x32_bf16 v[178:181], v[178:181], v[170:173], v[136:139]
	v_mfma_f32_16x16x32_bf16 v[150:153], v[150:153], v[170:173], v[140:143]
	v_add_u32_e32 v170, s33, v234
	v_add_u32_e32 v171, s33, v231
	v_add_u32_e32 v172, s33, v227
	v_add_u32_e32 v173, s33, v229
	ds_read_b64_tr_b16 v[140:141], v170
	ds_read_b64_tr_b16 v[142:143], v171
	ds_read_b64_tr_b16 v[136:137], v172
	ds_read_b64_tr_b16 v[138:139], v173
	ds_read_b64_tr_b16 v[132:133], v170 offset:2048
	ds_read_b64_tr_b16 v[134:135], v171 offset:2048
	ds_read_b64_tr_b16 v[128:129], v172 offset:2048
	ds_read_b64_tr_b16 v[130:131], v173 offset:2048
	ds_read_b64_tr_b16 v[124:125], v170 offset:4096
	ds_read_b64_tr_b16 v[126:127], v171 offset:4096
	ds_read_b64_tr_b16 v[120:121], v172 offset:4096
	ds_read_b64_tr_b16 v[122:123], v173 offset:4096
	ds_read_b64_tr_b16 v[112:113], v170 offset:6144
	ds_read_b64_tr_b16 v[114:115], v171 offset:6144
	ds_read_b64_tr_b16 v[100:101], v172 offset:6144
	ds_read_b64_tr_b16 v[102:103], v173 offset:6144
	s_waitcnt lgkmcnt(0)
	s_cselect_b32 s33, s1, 0
	v_mfma_f32_16x16x32_bf16 v[56:59], v[136:139], v[68:71], v[56:59]
	s_lshl_b32 s0, s33, 14
	s_add_i32 s1, s0, 0xffffc000
	s_cmp_lg_u32 s33, 0
	v_mfma_f32_16x16x32_bf16 v[52:55], v[140:143], v[68:71], v[52:55]
	s_cselect_b32 s1, s1, 0x10000
	s_add_i32 s1, s1, 0
	s_waitcnt vmcnt(3)
	v_mfma_f32_16x16x32_bf16 v[56:59], v[128:131], v[72:75], v[56:59]
	s_add_i32 s1, s1, s44
	s_barrier
	v_mfma_f32_16x16x32_bf16 v[52:55], v[132:135], v[72:75], v[52:55]
	s_add_i32 m0, s1, 0x10000
	s_add_i32 s0, s86, s0
	v_mfma_f32_16x16x32_bf16 v[56:59], v[120:123], v[76:79], v[56:59]
	v_add_u32_e32 v120, s0, v242
	s_add_i32 s1, s0, 0x2000
	s_add_i32 s38, s33, 1
	v_mfma_f32_16x16x32_bf16 v[52:55], v[124:127], v[76:79], v[52:55]
	s_cmp_lg_u32 s33, 4
	v_mfma_f32_16x16x32_bf16 v[56:59], v[100:103], v[80:83], v[56:59]
	v_lshl_add_u64 v[100:101], v[148:149], 0, s[16:17]
	global_load_lds_dwordx4 v[100:101], off
	v_mfma_f32_16x16x32_bf16 v[52:55], v[112:115], v[80:83], v[52:55]
	ds_read_b128 v[170:173], v236 offset:58368
	ds_read_b128 v[186:189], v236 offset:57344
	ds_read_b128 v[100:103], v120
	ds_read_b128 v[112:115], v120 offset:1024
	ds_read_b128 v[190:193], v120 offset:2048
	ds_read_b128 v[194:197], v120 offset:3072
	v_add_u32_e32 v120, s0, v243
	ds_read_b128 v[202:205], v120 offset:8192
	ds_read_b128 v[208:211], v120 offset:9216
	s_waitcnt lgkmcnt(0)
	v_mfma_f32_16x16x32_bf16 v[140:143], v[202:205], v[100:103], v[144:147]
	v_mfma_f32_16x16x32_bf16 v[238:241], v[186:189], v[100:103], v[116:119]
	v_mfma_f32_16x16x32_bf16 v[132:135], v[208:211], v[100:103], v[104:107]
	v_mfma_f32_16x16x32_bf16 v[136:139], v[170:173], v[100:103], v[84:87]
	v_mfma_f32_16x16x32_bf16 v[104:107], v[202:205], v[112:115], v[88:91]
	v_mfma_f32_16x16x32_bf16 v[100:103], v[186:189], v[112:115], v[92:95]
	v_mfma_f32_16x16x32_bf16 v[124:127], v[208:211], v[112:115], v[96:99]
	v_mfma_f32_16x16x32_bf16 v[128:131], v[170:173], v[112:115], v[158:161]
	v_mfma_f32_16x16x32_bf16 v[120:123], v[186:189], v[190:193], v[162:165]
	v_mfma_f32_16x16x32_bf16 v[116:119], v[170:173], v[190:193], v[166:169]
	v_mfma_f32_16x16x32_bf16 v[92:95], v[202:205], v[194:197], v[174:177]
	v_mfma_f32_16x16x32_bf16 v[96:99], v[186:189], v[194:197], v[154:157]
	s_nop 1
	v_add_u32_e32 v176, s1, v234
	v_add_u32_e32 v177, s1, v231
	v_mov_b32_e32 v231, v3
	v_mfma_f32_16x16x32_bf16 v[84:87], v[208:211], v[194:197], v[178:181]
	v_mfma_f32_16x16x32_bf16 v[88:91], v[170:173], v[194:197], v[150:153]
	s_nop 1
	v_add_u32_e32 v178, s1, v227
	v_add_u32_e32 v179, s1, v229
	ds_read_b64_tr_b16 v[172:173], v176
	ds_read_b64_tr_b16 v[174:175], v177
	ds_read_b64_tr_b16 v[168:169], v178
	ds_read_b64_tr_b16 v[170:171], v179
	ds_read_b64_tr_b16 v[164:165], v176 offset:2048
	ds_read_b64_tr_b16 v[166:167], v177 offset:2048
	ds_read_b64_tr_b16 v[160:161], v178 offset:2048
	ds_read_b64_tr_b16 v[162:163], v179 offset:2048
	ds_read_b64_tr_b16 v[156:157], v176 offset:4096
	ds_read_b64_tr_b16 v[158:159], v177 offset:4096
	ds_read_b64_tr_b16 v[152:153], v178 offset:4096
	ds_read_b64_tr_b16 v[154:155], v179 offset:4096
	ds_read_b64_tr_b16 v[148:149], v176 offset:6144
	ds_read_b64_tr_b16 v[150:151], v177 offset:6144
	ds_read_b64_tr_b16 v[144:145], v178 offset:6144
	ds_read_b64_tr_b16 v[146:147], v179 offset:6144
	s_waitcnt lgkmcnt(0)
; #define RC_MFMA(b, a, c) __builtin_amdgcn_mfma_f32_16x16x32_bf16((b), (a), (c), 0, 0, 0)
; template <int VAR  >
; __device__ __forceinline__ void ret_core_mfma(const bf16* P, const bf16* VT, const float* decay_logit  , bf16* YF, bf16* YB, float* PT, LAS unsigned char* lds, const int tid, const int bid, const int G) {
;     ...
;                 for (int m = 0; m < 4; ++m)
; #pragma unroll
;                     for (int n = 0; n < 2; ++n) { accA[m][n] = RC_MFMA(Bk[n], At[m], accA[m][n]); accY[m][n] = RC_MFMA(Bs[n], At[m], accY[m][n]); }
;                 { const unsigned kb = (unsigned)(size_t)(sq + 8192);
;                   const unsigned a0 = kb + trA, a1 = kb + trB, b0 = kb + (trA ^ 32u), b1 = kb + (trB ^ 32u);
;                   v2u l0, h0, l1, h1, l2, h2, l3, h3, p0, q0, p1, q1, p2, q2, p3, q3;
;                   asm volatile("ds_read_b64_tr_b16 %0, %16\n\tds_read_b64_tr_b16 %1, %17\n\tds_read_b64_tr_b16 %8, %18\n\tds_read_b64_tr_b16 %9, %19\n\t"
;                                "ds_read_b64_tr_b16 %2, %16 offset:2048\n\tds_read_b64_tr_b16 %3, %17 offset:2048\n\tds_read_b64_tr_b16 %10, %18 offset:2048\n\tds_read_b64_tr_b16 %11, %19 offset:2048\n\t"
;                                "ds_read_b64_tr_b16 %4, %16 offset:4096\n\tds_read_b64_tr_b16 %5, %17 offset:4096\n\tds_read_b64_tr_b16 %12, %18 offset:4096\n\tds_read_b64_tr_b16 %13, %19 offset:4096\n\t"
;                                "ds_read_b64_tr_b16 %6, %16 offset:6144\n\tds_read_b64_tr_b16 %7, %17 offset:6144\n\tds_read_b64_tr_b16 %14, %18 offset:6144\n\tds_read_b64_tr_b16 %15, %19 offset:6144\n\ts_waitcnt lgkmcnt(0)"
;                                : "=&v"(l0), "=&v"(h0), "=&v"(l1), "=&v"(h1), "=&v"(l2), "=&v"(h2), "=&v"(l3), "=&v"(h3), "=&v"(p0), "=&v"(q0), "=&v"(p1), "=&v"(q1), "=&v"(p2), "=&v"(q2), "=&v"(p3), "=&v"(q3)
;                                : "v"(a0), "v"(a1), "v"(b0), "v"(b1) : "memory");
;                   acc4[2 * ks] = RC_MFMA(__builtin_bit_cast(bf16x8v, ((v4u){l0.x, l0.y, h0.x, h0.y})), Avs[0], acc4[2 * ks]); acc4[2 * ks + 1] = RC_MFMA(__builtin_bit_cast(bf16x8v, ((v4u){p0.x, p0.y, q0.x, q0.y})), Avs[0], acc4[2 * ks + 1]);
;                   acc4[2 * ks] = RC_MFMA(__builtin_bit_cast(bf16x8v, ((v4u){l1.x, l1.y, h1.x, h1.y})), Avs[1], acc4[2 * ks]); acc4[2 * ks + 1] = RC_MFMA(__builtin_bit_cast(bf16x8v, ((v4u){p1.x, p1.y, q1.x, q1.y})), Avs[1], acc4[2 * ks + 1]);
	v_mfma_f32_16x16x32_bf16 v[112:115], v[202:205], v[190:193], v[108:111]
	v_ashrrev_i32_e32 v229, 31, v228
	v_ashrrev_i32_e32 v227, 31, v226
	v_mfma_f32_16x16x32_bf16 v[60:63], v[172:175], v[68:71], v[60:63]
	v_mfma_f32_16x16x32_bf16 v[64:67], v[168:171], v[68:71], v[64:67]
	v_mfma_f32_16x16x32_bf16 v[60:63], v[164:167], v[72:75], v[60:63]
	v_mfma_f32_16x16x32_bf16 v[64:67], v[160:163], v[72:75], v[64:67]
	v_mfma_f32_16x16x32_bf16 v[60:63], v[156:159], v[76:79], v[60:63]
	v_mfma_f32_16x16x32_bf16 v[64:67], v[152:155], v[76:79], v[64:67]
	v_mfma_f32_16x16x32_bf16 v[60:63], v[148:151], v[80:83], v[60:63]
	v_or_b32_e32 v149, s77, v2
	v_lshlrev_b32_e32 v68, 2, v149
	v_add_u32_e32 v69, s35, v68
	v_mfma_f32_16x16x32_bf16 v[64:67], v[144:147], v[80:83], v[64:67]
	v_lshl_add_u32 v144, v215, 2, s82
	ds_read_b32 v72, v69
	v_add_u32_e32 v68, s64, v68
	ds_read_b32 v150, v68
	v_lshl_add_u32 v68, v144, 2, s65
	ds_read_b128 v[76:79], v68
	s_waitcnt lgkmcnt(0)
	v_pk_mul_f32 v[70:71], v[240:241], v[72:73] op_sel_hi:[1,0]
	v_pk_mul_f32 v[68:69], v[238:239], v[72:73] op_sel_hi:[1,0]
	v_sub_u32_e32 v73, v144, v149
	v_sub_u32_e32 v74, v149, v144
	v_cndmask_b32_e64 v73, v73, v74, s[4:5]
	v_cmp_lt_i32_e32 vcc, -1, v73
	v_mul_f32_e32 v73, v150, v76
	v_mul_f32_e32 v73, v140, v73
	v_or_b32_e32 v145, 1, v144
	v_cndmask_b32_e32 v140, 0, v73, vcc
	v_sub_u32_e32 v73, v145, v149
	v_sub_u32_e32 v74, v149, v145
	v_cndmask_b32_e64 v73, v73, v74, s[4:5]
	v_cmp_lt_i32_e64 s[0:1], -1, v73
	v_mul_f32_e32 v73, v150, v77
	v_mul_f32_e32 v73, v141, v73
	v_or_b32_e32 v146, 2, v144
	v_cndmask_b32_e64 v141, 0, v73, s[0:1]
	v_sub_u32_e32 v73, v146, v149
	v_sub_u32_e32 v74, v149, v146
	v_cndmask_b32_e64 v73, v73, v74, s[4:5]
	v_cmp_lt_i32_e64 s[0:1], -1, v73
	v_mul_f32_e32 v73, v150, v78
	v_mul_f32_e32 v73, v142, v73
	v_or_b32_e32 v147, 3, v144
	v_cndmask_b32_e64 v142, 0, v73, s[0:1]
	v_sub_u32_e32 v73, v147, v149
	v_sub_u32_e32 v74, v149, v147
	v_cndmask_b32_e64 v73, v73, v74, s[4:5]
	v_cmp_lt_i32_e64 s[0:1], -1, v73
	v_mul_f32_e32 v73, v150, v79
	v_mul_f32_e32 v73, v143, v73
	v_add_u32_e32 v148, 16, v144
	v_cndmask_b32_e64 v143, 0, v73, s[0:1]
	v_lshl_add_u32 v73, v148, 2, s65
	ds_read_b128 v[80:83], v73
	v_pk_mul_f32 v[74:75], v[138:139], v[72:73] op_sel_hi:[1,0]
	v_pk_mul_f32 v[72:73], v[136:137], v[72:73] op_sel_hi:[1,0]
	v_sub_u32_e32 v136, v148, v149
	v_sub_u32_e32 v137, v149, v148
	v_cndmask_b32_e64 v136, v136, v137, s[4:5]
	v_cmp_lt_i32_e64 s[0:1], -1, v136
	s_waitcnt lgkmcnt(0)
	v_mul_f32_e32 v136, v150, v80
	v_add_u32_e32 v138, 17, v144
	v_mul_f32_e32 v132, v132, v136
	v_sub_u32_e32 v136, v138, v149
	v_sub_u32_e32 v137, v149, v138
	v_cndmask_b32_e64 v136, v136, v137, s[4:5]
	v_cndmask_b32_e64 v132, 0, v132, s[0:1]
	v_cmp_lt_i32_e64 s[0:1], -1, v136
	v_mul_f32_e32 v136, v150, v81
	v_add_u32_e32 v137, 18, v144
	v_mul_f32_e32 v133, v133, v136
	v_sub_u32_e32 v136, v137, v149
	v_sub_u32_e32 v139, v149, v137
	v_cndmask_b32_e64 v136, v136, v139, s[4:5]
	v_cndmask_b32_e64 v133, 0, v133, s[0:1]
	v_cmp_lt_i32_e64 s[0:1], -1, v136
	v_mul_f32_e32 v136, v150, v82
	v_mul_f32_e32 v134, v134, v136
	v_add_u32_e32 v136, 19, v144
	v_sub_u32_e32 v139, v136, v149
	v_sub_u32_e32 v151, v149, v136
	v_cndmask_b32_e64 v139, v139, v151, s[4:5]
	v_cndmask_b32_e64 v134, 0, v134, s[0:1]
	v_cmp_lt_i32_e64 s[0:1], -1, v139
	v_mul_f32_e32 v139, v150, v83
	v_or_b32_e32 v153, 16, v149
	v_mul_f32_e32 v135, v135, v139
	v_lshlrev_b32_e32 v139, 2, v153
	v_add_u32_e32 v150, s35, v139
	v_add_u32_e32 v139, s64, v139
	ds_read_b32 v154, v150
	ds_read_b32 v155, v139
	v_sub_u32_e32 v139, v144, v153
	v_sub_u32_e32 v150, v153, v144
	v_cndmask_b32_e64 v139, v139, v150, s[4:5]
	v_cndmask_b32_e64 v135, 0, v135, s[0:1]
	v_cmp_lt_i32_e64 s[0:1], -1, v139
	s_waitcnt lgkmcnt(0)
	v_mul_f32_e32 v139, v76, v155
	v_mul_f32_e32 v104, v104, v139
	v_cndmask_b32_e64 v139, 0, v104, s[0:1]
	v_sub_u32_e32 v104, v145, v153
	v_sub_u32_e32 v150, v153, v145
	v_cndmask_b32_e64 v104, v104, v150, s[4:5]
	v_cmp_lt_i32_e64 s[0:1], -1, v104
	v_mul_f32_e32 v104, v77, v155
	v_mul_f32_e32 v104, v105, v104
	v_cndmask_b32_e64 v150, 0, v104, s[0:1]
	v_sub_u32_e32 v104, v146, v153
	v_sub_u32_e32 v105, v153, v146
	v_cndmask_b32_e64 v104, v104, v105, s[4:5]
	v_cmp_lt_i32_e64 s[0:1], -1, v104
	v_mul_f32_e32 v104, v78, v155
	v_mul_f32_e32 v104, v106, v104
	v_cndmask_b32_e64 v151, 0, v104, s[0:1]
	v_sub_u32_e32 v104, v147, v153
	v_sub_u32_e32 v105, v153, v147
	v_cndmask_b32_e64 v104, v104, v105, s[4:5]
	v_cmp_lt_i32_e64 s[0:1], -1, v104
	v_mul_f32_e32 v104, v79, v155
	v_mul_f32_e32 v104, v107, v104
	v_cndmask_b32_e64 v152, 0, v104, s[0:1]
	v_pk_mul_f32 v[104:105], v[128:129], v[154:155] op_sel_hi:[1,0]
	v_mul_f32_e32 v128, v80, v155
	v_mul_f32_e32 v124, v124, v128
	v_cndmask_b32_e32 v128, 0, v124, vcc
	v_sub_u32_e32 v124, v138, v153
	v_sub_u32_e32 v129, v153, v138
	v_cndmask_b32_e64 v124, v124, v129, s[4:5]
	v_cmp_lt_i32_e32 vcc, -1, v124
	v_mul_f32_e32 v124, v81, v155
	v_mul_f32_e32 v124, v125, v124
	v_cndmask_b32_e32 v125, 0, v124, vcc
	v_sub_u32_e32 v124, v137, v153
	v_sub_u32_e32 v129, v153, v137
	v_cndmask_b32_e64 v124, v124, v129, s[4:5]
	v_cmp_lt_i32_e32 vcc, -1, v124
	v_mul_f32_e32 v124, v82, v155
	v_mul_f32_e32 v124, v126, v124
	v_cndmask_b32_e32 v126, 0, v124, vcc
	v_sub_u32_e32 v124, v136, v153
	v_sub_u32_e32 v129, v153, v136
	v_cndmask_b32_e64 v124, v124, v129, s[4:5]
	v_pk_mul_f32 v[102:103], v[102:103], v[154:155] op_sel_hi:[1,0]
	v_pk_mul_f32 v[100:101], v[100:101], v[154:155] op_sel_hi:[1,0]
	v_pk_mul_f32 v[106:107], v[130:131], v[154:155] op_sel_hi:[1,0]
	v_cmp_lt_i32_e32 vcc, -1, v124
	v_mul_f32_e32 v124, v83, v155
	v_or_b32_e32 v154, 32, v149
	v_mul_f32_e32 v124, v127, v124
	v_lshlrev_b32_e32 v129, 2, v154
	v_cndmask_b32_e32 v127, 0, v124, vcc
	v_add_u32_e32 v124, s35, v129
	v_add_u32_e32 v129, s64, v129
	ds_read_b32 v124, v124
	ds_read_b32 v155, v129
	v_sub_u32_e32 v129, v144, v154
	v_sub_u32_e32 v130, v154, v144
	v_cndmask_b32_e64 v129, v129, v130, s[4:5]
	v_cmp_lt_i32_e32 vcc, -1, v129
	s_waitcnt lgkmcnt(0)
; #define LAS __attribute__((address_space(3)))
; __device__ __forceinline__ unsigned cvtpk(float lo, float hi) { f32x2_t v = {lo, hi}; bf16x2_t b = __builtin_convertvector(v, bf16x2_t); return __builtin_bit_cast(unsigned, b); }
; #define RC_WAITV(n) asm volatile("s_waitcnt vmcnt(" #n ")" ::: "memory")
; #define RC_WAITL() asm volatile("s_waitcnt lgkmcnt(0)" ::: "memory")
; #define RC_BAR() do { asm volatile("" ::: "memory"); __builtin_amdgcn_s_barrier(); asm volatile("" ::: "memory"); } while (0)
; template <int VAR  >
; __device__ __forceinline__ void ret_core_mfma(const bf16* P, const bf16* VT, const float* decay_logit  , bf16* YF, bf16* YB, float* PT, LAS unsigned char* lds, const int tid, const int bid, const int G) {
;     ...
;                 for (int n = 0; n < 2; ++n) { const int i = 64 * wr + 16 * m + frc;
;                     const float qdf = *(const LAS float*)(lds + RC_TB + 1536 + i * 4), rwf = *(const LAS float*)(lds + RC_TB + 512 + i * 4);
;                     const f32x4 clf = *(const LAS f32x4*)(lds + RC_TB + 1024 + (32 * wc + 16 * n + 4 * fqc) * 4);
;                     accY[m][n] = accY[m][n] * qdf;
; #pragma unroll
;                     for (int ii = 0; ii < 4; ++ii) { const int j = 32 * wc + 16 * n + 4 * fqc + ii; const int dd = dir ? j - i : i - j;
;                         accA[m][n][ii] = dd >= 0 ? accA[m][n][ii] * (rwf * clf[ii]) : 0.f; } }
;             RC_BAR();
; #pragma unroll
;             for (int m = 0; m < 4; ++m)
; #pragma unroll
;                 for (int n = 0; n < 2; ++n) { v2u pw; pw.x = cvtpk(accA[m][n][0], accA[m][n][1]); pw.y = cvtpk(accA[m][n][2], accA[m][n][3]);
;                     *(LAS v2u*)(lds + RC_ST + wc * 8192 + (4 * wr + m) * 1024 + sl_swz(frc * 64 + (16 * n + 4 * fqc) * 2)) = pw; }
; #pragma unroll
;             for (int js = 0; js < 4; ++js) vnx[js] = *(const v4u*)(vown + tokn + 32 * js + zo);
;             RC_WAITL();
; #pragma unroll
;             for (int js = 0; js < 4; ++js) {
;                 if (js == 0) RC_WAITV(7); else if (js == 1) RC_WAITV(8); else if (js == 2) RC_WAITV(9); else RC_WAITV(10);
;                 RC_BAR();
	v_mul_f32_e32 v129, v76, v155
	v_mul_f32_e32 v112, v112, v129
	v_cndmask_b32_e32 v129, 0, v112, vcc
	v_sub_u32_e32 v112, v145, v154
	v_sub_u32_e32 v130, v154, v145
	v_cndmask_b32_e64 v112, v112, v130, s[4:5]
	v_cmp_lt_i32_e32 vcc, -1, v112
	v_mul_f32_e32 v112, v77, v155
	v_mul_f32_e32 v112, v113, v112
	v_cndmask_b32_e32 v130, 0, v112, vcc
	v_sub_u32_e32 v112, v146, v154
	v_sub_u32_e32 v113, v154, v146
	v_cndmask_b32_e64 v112, v112, v113, s[4:5]
	v_cmp_lt_i32_e32 vcc, -1, v112
	v_mul_f32_e32 v112, v78, v155
	v_mul_f32_e32 v112, v114, v112
	v_cndmask_b32_e32 v131, 0, v112, vcc
	v_sub_u32_e32 v112, v147, v154
	v_sub_u32_e32 v113, v154, v147
	v_cndmask_b32_e64 v112, v112, v113, s[4:5]
	v_cmp_lt_i32_e32 vcc, -1, v112
	v_mul_f32_e32 v112, v79, v155
	v_mfma_f32_16x16x32_bf16 v[108:111], v[208:211], v[190:193], v[182:185]
	v_mul_f32_e32 v112, v115, v112
	v_cndmask_b32_e32 v153, 0, v112, vcc
	v_pk_mul_f32 v[112:113], v[116:117], v[124:125] op_sel_hi:[1,0]
	v_sub_u32_e32 v116, v148, v154
	v_sub_u32_e32 v117, v154, v148
	v_cndmask_b32_e64 v116, v116, v117, s[4:5]
	v_cmp_lt_i32_e32 vcc, -1, v116
	v_mul_f32_e32 v116, v80, v155
	v_mul_f32_e32 v108, v108, v116
	v_sub_u32_e32 v116, v138, v154
	v_sub_u32_e32 v117, v154, v138
	v_cndmask_b32_e64 v116, v116, v117, s[4:5]
	v_cndmask_b32_e32 v108, 0, v108, vcc
	v_cmp_lt_i32_e32 vcc, -1, v116
	v_mul_f32_e32 v116, v81, v155
	v_mul_f32_e32 v109, v109, v116
	v_sub_u32_e32 v116, v137, v154
	v_sub_u32_e32 v117, v154, v137
	v_cndmask_b32_e64 v116, v116, v117, s[4:5]
	v_cndmask_b32_e32 v109, 0, v109, vcc
	v_cmp_lt_i32_e32 vcc, -1, v116
	v_mul_f32_e32 v116, v82, v155
	v_mul_f32_e32 v110, v110, v116
	v_sub_u32_e32 v116, v136, v154
	v_sub_u32_e32 v117, v154, v136
	v_cndmask_b32_e64 v116, v116, v117, s[4:5]
	v_or_b32_e32 v117, 48, v149
	v_pk_mul_f32 v[114:115], v[118:119], v[124:125] op_sel_hi:[1,0]
	v_cndmask_b32_e32 v110, 0, v110, vcc
	v_cmp_lt_i32_e32 vcc, -1, v116
	v_mul_f32_e32 v116, v83, v155
	v_lshlrev_b32_e32 v118, 2, v117
	v_mul_f32_e32 v111, v111, v116
	v_add_u32_e32 v116, s35, v118
	v_add_u32_e32 v118, s64, v118
	ds_read_b32 v116, v116
	ds_read_b32 v118, v118
	v_pk_mul_f32 v[122:123], v[122:123], v[124:125] op_sel_hi:[1,0]
	v_pk_mul_f32 v[120:121], v[120:121], v[124:125] op_sel_hi:[1,0]
	v_sub_u32_e32 v119, v144, v117
	v_sub_u32_e32 v124, v117, v144
	v_cndmask_b32_e64 v119, v119, v124, s[4:5]
	s_waitcnt lgkmcnt(0)
	v_mul_f32_e32 v76, v76, v118
	v_cndmask_b32_e32 v111, 0, v111, vcc
	v_cmp_lt_i32_e32 vcc, -1, v119
	v_mul_f32_e32 v76, v92, v76
	v_sub_u32_e32 v92, v117, v145
	v_cndmask_b32_e32 v119, 0, v76, vcc
	v_sub_u32_e32 v76, v145, v117
	v_cndmask_b32_e64 v76, v76, v92, s[4:5]
	v_cmp_lt_i32_e32 vcc, -1, v76
	v_mul_f32_e32 v76, v77, v118
	v_mul_f32_e32 v76, v93, v76
	v_cndmask_b32_e32 v124, 0, v76, vcc
	v_sub_u32_e32 v76, v146, v117
	v_sub_u32_e32 v77, v117, v146
	v_cndmask_b32_e64 v76, v76, v77, s[4:5]
	v_cmp_lt_i32_e32 vcc, -1, v76
	v_mul_f32_e32 v76, v78, v118
	v_mul_f32_e32 v76, v94, v76
	v_cndmask_b32_e32 v78, 0, v76, vcc
	v_sub_u32_e32 v76, v147, v117
	v_sub_u32_e32 v77, v117, v147
	v_cndmask_b32_e64 v76, v76, v77, s[4:5]
	v_cmp_lt_i32_e32 vcc, -1, v76
	v_mul_f32_e32 v76, v79, v118
	v_mul_f32_e32 v76, v95, v76
	v_cndmask_b32_e32 v79, 0, v76, vcc
	v_sub_u32_e32 v76, v148, v117
	v_sub_u32_e32 v77, v117, v148
	v_cndmask_b32_e64 v76, v76, v77, s[4:5]
	v_cmp_lt_i32_e32 vcc, -1, v76
	v_mul_f32_e32 v76, v80, v118
	v_mul_f32_e32 v76, v84, v76
	v_cndmask_b32_e32 v80, 0, v76, vcc
	v_sub_u32_e32 v76, v138, v117
	v_sub_u32_e32 v77, v117, v138
	v_cndmask_b32_e64 v76, v76, v77, s[4:5]
	v_cmp_lt_i32_e32 vcc, -1, v76
	v_mul_f32_e32 v76, v81, v118
	v_mul_f32_e32 v76, v85, v76
	v_cndmask_b32_e32 v81, 0, v76, vcc
	v_sub_u32_e32 v76, v137, v117
	v_sub_u32_e32 v77, v117, v137
	v_cndmask_b32_e64 v76, v76, v77, s[4:5]
	v_cmp_lt_i32_e32 vcc, -1, v76
	v_mul_f32_e32 v76, v82, v118
	v_mul_f32_e32 v76, v86, v76
	v_lshl_add_u32 v84, v2, 6, v226
	v_cndmask_b32_e32 v82, 0, v76, vcc
	v_sub_u32_e32 v76, v136, v117
	v_sub_u32_e32 v77, v117, v136
	v_lshrrev_b32_e32 v85, 4, v84
	v_cndmask_b32_e64 v76, v76, v77, s[4:5]
	v_and_b32_e32 v85, 32, v85
	v_cmp_lt_i32_e32 vcc, -1, v76
	v_mul_f32_e32 v76, v83, v118
	v_xad_u32 v85, v85, v84, s83
	v_add_u32_e32 v84, 32, v84
	v_mul_f32_e32 v76, v87, v76
	v_lshrrev_b32_e32 v86, 4, v84
	v_cndmask_b32_e32 v83, 0, v76, vcc
	v_cvt_pk_bf16_f32 v76, v140, v141
	v_cvt_pk_bf16_f32 v77, v142, v143
	v_and_b32_e32 v86, 32, v86
	ds_write_b64 v85, v[76:77]
	v_cvt_pk_bf16_f32 v76, v132, v133
	v_cvt_pk_bf16_f32 v77, v134, v135
	v_xad_u32 v84, v86, v84, s83
	ds_write_b64 v84, v[76:77]
	v_cvt_pk_bf16_f32 v76, v139, v150
	v_cvt_pk_bf16_f32 v77, v151, v152
	ds_write_b64 v85, v[76:77] offset:1024
	v_cvt_pk_bf16_f32 v76, v128, v125
	v_cvt_pk_bf16_f32 v77, v126, v127
	ds_write_b64 v84, v[76:77] offset:1024
	v_cvt_pk_bf16_f32 v76, v129, v130
	v_cvt_pk_bf16_f32 v77, v131, v153
	ds_write_b64 v85, v[76:77] offset:2048
	v_cvt_pk_bf16_f32 v76, v108, v109
	v_cvt_pk_bf16_f32 v77, v110, v111
	s_cselect_b32 s0, s38, 0
	ds_write_b64 v84, v[76:77] offset:2048
	v_cvt_pk_bf16_f32 v76, v119, v124
	v_cvt_pk_bf16_f32 v77, v78, v79
	s_lshl_b32 s40, s7, 7
	ds_write_b64 v85, v[76:77] offset:3072
	v_cvt_pk_bf16_f32 v76, v80, v81
	v_cvt_pk_bf16_f32 v77, v82, v83
	s_ashr_i32 s41, s40, 31
	s_lshl_b32 s1, s0, 14
	ds_write_b64 v84, v[76:77] offset:3072
	v_lshl_add_u64 v[76:77], s[40:41], 1, v[222:223]
	s_lshl_b64 s[40:41], s[40:41], 12
	s_add_i32 s7, s1, 0xc000
	v_lshl_add_u64 v[80:81], v[228:229], 1, v[76:77]
	s_cmp_lg_u32 s0, 0
	v_pk_mul_f32 v[94:95], v[90:91], v[116:117] op_sel_hi:[1,0]
	v_pk_mul_f32 v[92:93], v[88:89], v[116:117] op_sel_hi:[1,0]
	global_load_dwordx4 v[88:91], v[80:81], off
	global_load_dwordx4 v[84:87], v[80:81], off offset:64
	global_load_dwordx4 v[76:79], v[80:81], off offset:128
	s_nop 0
	global_load_dwordx4 v[80:83], v[80:81], off offset:192
	s_waitcnt lgkmcnt(0)
	s_cselect_b32 s7, s7, 0x20000
	s_waitcnt vmcnt(7)
	s_add_i32 s7, s45, s7
	s_barrier
; #define LAS __attribute__((address_space(3)))
; #define RC_WAITV(n) asm volatile("s_waitcnt vmcnt(" #n ")" ::: "memory")
; #define RC_WAITL() asm volatile("s_waitcnt lgkmcnt(0)" ::: "memory")
; #define RC_BAR() do { asm volatile("" ::: "memory"); __builtin_amdgcn_s_barrier(); asm volatile("" ::: "memory"); } while (0)
; #define RC_MFMA(b, a, c) __builtin_amdgcn_mfma_f32_16x16x32_bf16((b), (a), (c), 0, 0, 0)
; #define RC_ISSUE(st, tk, sl) do { if ((st) < 8) { const size_t to_ = (size_t)(tk) * RQK + 32 * (st); RC_DMA(qsrc + to_, RC_RG + (sl) * 16384 + w * 1024); RC_DMA(ksrc + to_, RC_RG + (sl) * 16384 + 8192 + w * 1024); } \
;                                   else RC_DMA(vsrc + (tk) + 32 * ((st) - 8), RC_RG + (sl) * 16384 + w * 1024); } while (0)
; template <int VAR  >
; __device__ __forceinline__ void ret_core_mfma(const bf16* P, const bf16* VT, const float* decay_logit  , bf16* YF, bf16* YB, float* PT, LAS unsigned char* lds, const int tid, const int bid, const int G) {
;     ...
; #pragma unroll
;             for (int js = 0; js < 4; ++js) {
;                 if (js == 0) RC_WAITV(7); else if (js == 1) RC_WAITV(8); else if (js == 2) RC_WAITV(9); else RC_WAITV(10);
;                 RC_BAR();
;                 { const int s4 = RC_PREV(slot); RC_ISSUE(js, tokn, s4); }
;                 bf16x8v At[4], Bv[2];
;                 const LAS unsigned char* sv = lds + RC_RG + slot * 16384;
; #pragma unroll
;                 for (int m = 0; m < 4; ++m) At[m] = *(const LAS bf16x8v*)(lds + RC_ST + js * 8192 + aoff + m * 1024);
; #pragma unroll
;                 for (int n = 0; n < 2; ++n) Bv[n] = *(const LAS bf16x8v*)(sv + boff + n * 1024);
;                 RC_WAITL();
; #pragma unroll
;                 for (int m = 0; m < 4; ++m)
; #pragma unroll
;                     for (int n = 0; n < 2; ++n) accY[m][n] = RC_MFMA(Bv[n], At[m], accY[m][n]);
;                 slot = RC_NEXT(slot);
;             }
	v_lshl_add_u64 v[108:109], v[218:219], 0, s[40:41]
	s_mov_b32 m0, s7
	v_lshl_add_u64 v[110:111], v[108:109], 0, s[62:63]
	global_load_lds_dwordx4 v[108:109], off
	s_add_i32 m0, s7, 0x2000
	v_add_u32_e32 v144, 0, v242
	global_load_lds_dwordx4 v[110:111], off
	v_add_u32_e32 v110, s1, v251
	s_add_i32 s1, s0, 1
	s_cmp_lg_u32 s0, 4
	s_cselect_b32 s0, s1, 0
	v_pk_mul_f32 v[98:99], v[98:99], v[116:117] op_sel_hi:[1,0]
	v_pk_mul_f32 v[96:97], v[96:97], v[116:117] op_sel_hi:[1,0]
	ds_read_b128 v[116:119], v144
	ds_read_b128 v[124:127], v144 offset:1024
	ds_read_b128 v[128:131], v144 offset:2048
	ds_read_b128 v[132:135], v144 offset:3072
	ds_read_b128 v[136:139], v110
	ds_read_b128 v[140:143], v110 offset:1024
	s_lshl_b32 s1, s0, 14
	s_add_i32 s7, s1, 0xc000
	s_cmp_lg_u32 s0, 0
	s_waitcnt lgkmcnt(0)
	s_cselect_b32 s7, s7, 0x20000
	s_waitcnt vmcnt(8)
	s_add_i32 s7, s45, s7
	s_waitcnt lgkmcnt(0)
	v_mfma_f32_16x16x32_bf16 v[110:113], v[140:143], v[128:131], v[112:115]
	s_barrier
	s_mov_b32 m0, s7
	v_mfma_f32_16x16x32_bf16 v[68:71], v[136:139], v[116:119], v[68:71]
	v_lshl_add_u64 v[114:115], v[108:109], 0, 64
	global_load_lds_dwordx4 v[114:115], off
	v_lshl_add_u64 v[114:115], v[108:109], 0, s[72:73]
	s_add_i32 m0, s7, 0x2000
	v_mfma_f32_16x16x32_bf16 v[72:75], v[140:143], v[116:119], v[72:75]
	global_load_lds_dwordx4 v[114:115], off
	v_add_u32_e32 v114, s1, v251
	s_add_i32 s1, s0, 1
	s_cmp_lg_u32 s0, 4
	s_cselect_b32 s0, s1, 0
	s_lshl_b32 s1, s0, 14
	v_mfma_f32_16x16x32_bf16 v[100:103], v[136:139], v[124:127], v[100:103]
	s_add_i32 s7, s1, 0xc000
	s_cmp_lg_u32 s0, 0
	s_cselect_b32 s7, s7, 0x20000
	v_mfma_f32_16x16x32_bf16 v[104:107], v[140:143], v[124:127], v[104:107]
	s_add_i32 s7, s45, s7
	s_mov_b32 m0, s7
	v_mfma_f32_16x16x32_bf16 v[116:119], v[136:139], v[128:131], v[120:123]
	v_mfma_f32_16x16x32_bf16 v[96:99], v[136:139], v[132:135], v[96:99]
	v_mfma_f32_16x16x32_bf16 v[92:95], v[140:143], v[132:135], v[92:95]
	s_nop 0
	ds_read_b128 v[120:123], v144 offset:8192
	ds_read_b128 v[124:127], v144 offset:9216
	ds_read_b128 v[128:131], v144 offset:10240
	ds_read_b128 v[132:135], v144 offset:11264
	ds_read_b128 v[136:139], v114
	ds_read_b128 v[140:143], v114 offset:1024
	s_waitcnt lgkmcnt(0)
	s_waitcnt vmcnt(9)
	s_waitcnt lgkmcnt(0)
	v_mfma_f32_16x16x32_bf16 v[114:117], v[136:139], v[128:131], v[116:119]
	s_barrier
	v_mfma_f32_16x16x32_bf16 v[68:71], v[136:139], v[120:123], v[68:71]
	s_nop 0
	v_lshl_add_u64 v[118:119], v[108:109], 0, s[66:67]
	global_load_lds_dwordx4 v[118:119], off
	v_mfma_f32_16x16x32_bf16 v[100:103], v[136:139], v[124:127], v[100:103]
	s_add_i32 m0, s7, 0x2000
	v_lshl_add_u64 v[118:119], v[108:109], 0, s[84:85]
	global_load_lds_dwordx4 v[118:119], off
	v_mfma_f32_16x16x32_bf16 v[96:99], v[136:139], v[132:135], v[96:99]
	v_add_u32_e32 v138, s1, v251
	s_add_i32 s1, s0, 1
	s_cmp_lg_u32 s0, 4
	s_cselect_b32 s7, s1, 0
	v_mfma_f32_16x16x32_bf16 v[72:75], v[140:143], v[120:123], v[72:75]
	s_lshl_b32 s0, s7, 14
	s_add_i32 s1, s0, 0xc000
	s_cmp_lg_u32 s7, 0
	v_mfma_f32_16x16x32_bf16 v[104:107], v[140:143], v[124:127], v[104:107]
	s_cselect_b32 s1, s1, 0x20000
	s_add_i32 s1, s45, s1
	s_mov_b32 m0, s1
	v_mfma_f32_16x16x32_bf16 v[110:113], v[140:143], v[128:131], v[110:113]
	v_mfma_f32_16x16x32_bf16 v[92:95], v[140:143], v[132:135], v[92:95]
	ds_read_b128 v[118:121], v144 offset:16384
	ds_read_b128 v[122:125], v144 offset:17408
	ds_read_b128 v[126:129], v144 offset:18432
	ds_read_b128 v[130:133], v144 offset:19456
	ds_read_b128 v[134:137], v138
	ds_read_b128 v[138:141], v138 offset:1024
	s_waitcnt lgkmcnt(0)
	s_waitcnt vmcnt(10)
	s_waitcnt lgkmcnt(0)
	v_mfma_f32_16x16x32_bf16 v[114:117], v[134:137], v[126:129], v[114:117]
	s_barrier
; template <int O> __device__ __forceinline__ float swz_xor(float v) { return __builtin_bit_cast(float, __builtin_amdgcn_ds_swizzle(__builtin_bit_cast(int, v), (O << 10) | 0x1f)); }
; __device__ __forceinline__ float get_xor32(float v, int lane) { return __builtin_bit_cast(float, __builtin_amdgcn_ds_bpermute((lane ^ 32) << 2, __builtin_bit_cast(int, v))); }
; __device__ __forceinline__ unsigned cvtpk(float lo, float hi) { f32x2_t v = {lo, hi}; bf16x2_t b = __builtin_convertvector(v, bf16x2_t); return __builtin_bit_cast(unsigned, b); }
; #define RC_MFMA(b, a, c) __builtin_amdgcn_mfma_f32_16x16x32_bf16((b), (a), (c), 0, 0, 0)
; template <int VAR  >
; __device__ __forceinline__ void ret_core_mfma(const bf16* P, const bf16* VT, const float* decay_logit  , bf16* YF, bf16* YB, float* PT, LAS unsigned char* lds, const int tid, const int bid, const int G) {
;     ...
; #pragma unroll
;                 for (int m = 0; m < 4; ++m)
; #pragma unroll
;                     for (int n = 0; n < 2; ++n) accY[m][n] = RC_MFMA(Bv[n], At[m], accY[m][n]);
;                 slot = RC_NEXT(slot);
;             }
; #pragma unroll
;             for (int m = 0; m < 4; ++m) { v4u pw; pw.x = cvtpk(accY[m][0][0], accY[m][0][1]); pw.y = cvtpk(accY[m][0][2], accY[m][0][3]); pw.z = cvtpk(accY[m][1][0], accY[m][1][1]); pw.w = cvtpk(accY[m][1][2], accY[m][1][3]);
;                 *(v4u*)(Y + (rowbase + tok0 + 64 * wr + 16 * m + frc + zo) * DV + h * DVR + es * 128 + 32 * wc + 8 * fqc) = pw; }
; #pragma unroll
;             for (int m = 0; m < 4; ++m) { float sv = 0.f, sq = 0.f;
; #pragma unroll
;                 for (int n = 0; n < 2; ++n)
; #pragma unroll
;                     for (int ii = 0; ii < 4; ++ii) { const float yv = accY[m][n][ii]; sv += yv; sq += yv * yv; }
;                 sv += swz_xor<16>(sv); sq += swz_xor<16>(sq); sv += get_xor32(sv, lc); sq += get_xor32(sq, lc);
;                 float* sp = PT + (((size_t)((h * 2 + dir) * 16 + es * 4 + wc)) * M + (rowbase + tok0 + 64 * wr + 16 * m + frc + zo)) * 2;
;                 if (fqc == 0) *(f32x2_t*)sp = (f32x2_t){sv, sq}; }
	v_mfma_f32_16x16x32_bf16 v[110:113], v[138:141], v[126:129], v[110:113]
	v_mfma_f32_16x16x32_bf16 v[126:129], v[138:141], v[130:133], v[92:95]
	s_nop 2
	v_lshl_add_u64 v[92:93], v[108:109], 0, s[16:17]
	global_load_lds_dwordx4 v[92:93], off
	v_lshl_add_u64 v[92:93], v[108:109], 0, s[18:19]
	s_add_i32 m0, s1, 0x2000
	v_mfma_f32_16x16x32_bf16 v[68:71], v[134:137], v[118:121], v[68:71]
	global_load_lds_dwordx4 v[92:93], off
	v_mfma_f32_16x16x32_bf16 v[72:75], v[138:141], v[118:121], v[72:75]
	v_mfma_f32_16x16x32_bf16 v[118:121], v[138:141], v[122:125], v[104:107]
	s_nop 2
	v_add_u32_e32 v104, s0, v251
	v_mfma_f32_16x16x32_bf16 v[100:103], v[134:137], v[122:125], v[100:103]
	s_add_u32 s0, s60, s53
	s_addc_u32 s1, s93, 0
	v_lshl_add_u64 v[108:109], s[0:1], 0, v[228:229]
	v_mfma_f32_16x16x32_bf16 v[122:125], v[134:137], v[130:133], v[96:99]
	ds_read_b128 v[92:95], v144 offset:24576
	s_nop 1
	ds_read_b128 v[96:99], v144 offset:25600
	ds_read_b128 v[130:133], v144 offset:26624
	ds_read_b128 v[134:137], v144 offset:27648
	ds_read_b128 v[138:141], v104
	ds_read_b128 v[142:145], v104 offset:1024
	s_waitcnt lgkmcnt(0)
	s_waitcnt lgkmcnt(0)
	v_mfma_f32_16x16x32_bf16 v[146:149], v[138:141], v[92:95], v[68:71]
	s_mov_b32 s0, 0x30000
	v_mfma_f32_16x16x32_bf16 v[150:153], v[142:145], v[92:95], v[72:75]
	v_mfma_f32_16x16x32_bf16 v[104:107], v[138:141], v[96:99], v[100:103]
	v_mfma_f32_16x16x32_bf16 v[100:103], v[142:145], v[96:99], v[118:121]
	v_mfma_f32_16x16x32_bf16 v[92:95], v[142:145], v[130:133], v[110:113]
	s_nop 2
	v_lshl_add_u64 v[112:113], v[108:109], 0, v[2:3]
	v_mfma_f32_16x16x32_bf16 v[96:99], v[138:141], v[130:133], v[114:117]
	v_lshlrev_b64 v[112:113], 12, v[112:113]
	v_cvt_pk_bf16_f32 v108, v146, v147
	v_cvt_pk_bf16_f32 v109, v148, v149
	v_lshl_add_u64 v[114:115], v[226:227], 1, s[54:55]
	v_lshl_add_u64 v[112:113], v[114:115], 0, v[112:113]
	v_cvt_pk_bf16_f32 v110, v150, v151
	v_cvt_pk_bf16_f32 v111, v152, v153
	v_add_co_u32_e32 v114, vcc, s58, v112
	v_mfma_f32_16x16x32_bf16 v[72:75], v[138:141], v[134:137], v[122:125]
	global_store_dwordx4 v[112:113], v[108:111], off
	v_addc_co_u32_e32 v115, vcc, 0, v113, vcc
	v_mfma_f32_16x16x32_bf16 v[68:71], v[142:145], v[134:137], v[126:129]
	v_cvt_pk_bf16_f32 v108, v104, v105
	v_cvt_pk_bf16_f32 v109, v106, v107
	v_cvt_pk_bf16_f32 v110, v100, v101
	v_cvt_pk_bf16_f32 v111, v102, v103
	global_store_dwordx4 v[114:115], v[108:111], off
	v_add_co_u32_e32 v114, vcc, s59, v112
	s_nop 0
	v_cvt_pk_bf16_f32 v108, v96, v97
	v_addc_co_u32_e32 v115, vcc, 0, v113, vcc
	v_cvt_pk_bf16_f32 v109, v98, v99
	v_cvt_pk_bf16_f32 v110, v92, v93
	v_cvt_pk_bf16_f32 v111, v94, v95
	v_add_co_u32_e32 v112, vcc, s0, v112
	global_store_dwordx4 v[114:115], v[108:111], off
	s_nop 0
	v_addc_co_u32_e32 v113, vcc, 0, v113, vcc
	v_cvt_pk_bf16_f32 v108, v72, v73
	v_cvt_pk_bf16_f32 v109, v74, v75
	v_cvt_pk_bf16_f32 v110, v68, v69
	v_cvt_pk_bf16_f32 v111, v70, v71
	global_store_dwordx4 v[112:113], v[108:111], off
	v_pk_mul_f32 v[112:113], v[146:147], v[146:147]
	v_pk_mul_f32 v[116:117], v[150:151], v[150:151]
	v_add_f32_e32 v110, 0, v146
	v_add_f32_e32 v110, v147, v110
	v_add_f32_e32 v115, v148, v110
	v_pk_mul_f32 v[110:111], v[148:149], v[148:149]
	v_fmac_f32_e32 v113, v146, v146
	v_add_f32_e32 v112, v110, v113
	v_add_f32_e32 v110, v149, v115
	v_mov_b32_e32 v148, v150
	v_add_f32_e32 v113, v150, v110
	v_pk_mul_f32 v[110:111], v[148:149], v[148:149]
	v_lshlrev_b32_e32 v108, 2, v230
	v_add_f32_e32 v111, v111, v112
	v_add_f32_e32 v111, v110, v111
	v_add_f32_e32 v110, v151, v113
	v_pk_mul_f32 v[112:113], v[152:153], v[152:153]
	v_add_f32_e32 v111, v117, v111
	v_add_f32_e32 v110, v152, v110
	v_add_f32_e32 v113, v112, v111
	v_mul_f32_e32 v111, v153, v153
	v_mov_b32_e32 v112, v153
	v_pk_add_f32 v[110:111], v[112:113], v[110:111]
	v_mov_b32_e32 v112, v110
	v_mov_b32_e32 v113, v111
	s_nop 1
	v_permlane16_swap_b32_e32 v112, v110
	v_permlane16_swap_b32_e32 v113, v111
	v_xor_b32_e32 v114, 0x80, v108
	v_lshl_add_u64 v[108:109], s[78:79], 0, v[230:231]
	v_lshl_add_u64 v[108:109], v[108:109], 0, v[228:229]
	v_lshl_add_u64 v[108:109], v[108:109], 0, s[60:61]
	s_waitcnt lgkmcnt(0)
	v_pk_add_f32 v[110:111], v[110:111], v[112:113]
	v_mov_b32_e32 v112, v110
	v_mov_b32_e32 v113, v111
	s_nop 1
	v_permlane32_swap_b32_e32 v112, v110
	v_permlane32_swap_b32_e32 v113, v111
	v_cmp_gt_u32_e32 vcc, 16, v230
	v_lshl_add_u64 v[108:109], v[108:109], 3, s[14:15]
	s_and_saveexec_b64 s[0:1], vcc
	s_cbranch_execz .LBB0_57
	s_waitcnt lgkmcnt(0)
	v_pk_add_f32 v[110:111], v[110:111], v[112:113]
	global_store_dwordx2 v[108:109], v[110:111], off

; #define LAS __attribute__((address_space(3)))
; __device__ __forceinline__ void attn_group_mfma5(const bf16* QK, const float* bias2g, int ldil, int first, bf16* OACC, float* LSE, LAS unsigned char* lds, const int tid, const int bid, const int G) {
;     ...
;         const LAS float* tb = tab + (32 + 4 * kq - n);
;         int kt0 = q4 * 128 - 64 + 16 * wq + 4 * kq; asm volatile("" : "+v"(kt0));
;         float mx = NEGBIG;
; #pragma unroll
;         for (int kb = 0; kb < 9; ++kb)
; #pragma unroll
;             for (int e = 0; e < 4; ++e) { const int krel = 16 * kb + e;
;                 float sv = S[kb][e] * SC + tb[krel]; sv = ((unsigned)(kt0 + krel) >= (unsigned)Ls) ? NEGBIG : sv; S[kb][e] = sv; mx = fmaxf(mx, sv); }
.LBB0_218:
	v_lshl_add_u32 v0, v73, 2, s1
	v_add_u32_e32 v84, 0x10080, v0
	v_add_u32_e32 v2, s36, v74
	ds_read2_b32 v[0:1], v84 offset1:1
	ds_read2_b32 v[86:87], v84 offset0:2 offset1:3
	v_cmp_gt_u32_e32 vcc, s33, v2
	s_waitcnt lgkmcnt(0)
	v_fmamk_f32 v0, v44, 0x3e38aa3b, v0
	v_mov_b32_e32 v44, s50
	v_fmac_f32_e32 v1, 0x3e38aa3b, v45
	v_add_u32_e32 v45, 1, v2
	v_cndmask_b32_e32 v0, v44, v0, vcc
	v_cmp_gt_u32_e32 vcc, s33, v45
	v_fmamk_f32 v45, v46, 0x3e38aa3b, v86
	v_add_u32_e32 v46, 2, v2
	v_cndmask_b32_e32 v1, v44, v1, vcc
	v_cmp_gt_u32_e32 vcc, s33, v46
	v_add_u32_e32 v46, 3, v2
	v_fmac_f32_e32 v87, 0x3e38aa3b, v47
	v_cndmask_b32_e32 v45, v44, v45, vcc
	v_cmp_gt_u32_e32 vcc, s33, v46
	v_max3_f32 v85, s50, v0, v1
	s_nop 0
	v_cndmask_b32_e32 v46, v44, v87, vcc
	ds_read2_b32 v[86:87], v84 offset0:16 offset1:17
	v_max3_f32 v47, v85, v45, v46
	v_add_u32_e32 v85, 16, v2
	v_cmp_gt_u32_e32 vcc, s33, v85
	v_add_u32_e32 v85, 18, v2
	s_waitcnt lgkmcnt(0)
	v_fmamk_f32 v40, v40, 0x3e38aa3b, v86
	v_fmac_f32_e32 v87, 0x3e38aa3b, v41
	v_add_u32_e32 v41, 17, v2
	v_cndmask_b32_e32 v40, v44, v40, vcc
	v_cmp_gt_u32_e32 vcc, s33, v41
	s_nop 1
	v_cndmask_b32_e32 v41, v44, v87, vcc
	ds_read2_b32 v[86:87], v84 offset0:18 offset1:19
	v_cmp_gt_u32_e32 vcc, s33, v85
	v_add_u32_e32 v85, 32, v2
	v_max3_f32 v47, v47, v40, v41
	s_waitcnt lgkmcnt(0)
	v_fmamk_f32 v42, v42, 0x3e38aa3b, v86
	v_fmac_f32_e32 v87, 0x3e38aa3b, v43
	v_add_u32_e32 v43, 19, v2
	v_cndmask_b32_e32 v42, v44, v42, vcc
	v_cmp_gt_u32_e32 vcc, s33, v43
	s_nop 1
	v_cndmask_b32_e32 v43, v44, v87, vcc
	ds_read2_b32 v[86:87], v84 offset0:32 offset1:33
	v_cmp_gt_u32_e32 vcc, s33, v85
	v_add_u32_e32 v85, 34, v2
	v_max3_f32 v47, v47, v42, v43
	s_waitcnt lgkmcnt(0)
	v_fmamk_f32 v36, v36, 0x3e38aa3b, v86
	v_fmac_f32_e32 v87, 0x3e38aa3b, v37
	v_add_u32_e32 v37, 33, v2
	v_cndmask_b32_e32 v36, v44, v36, vcc
	v_cmp_gt_u32_e32 vcc, s33, v37
	s_nop 1
	v_cndmask_b32_e32 v37, v44, v87, vcc
	ds_read2_b32 v[86:87], v84 offset0:34 offset1:35
	v_cmp_gt_u32_e32 vcc, s33, v85
	v_add_u32_e32 v85, 48, v2
	v_max3_f32 v47, v47, v36, v37
	s_waitcnt lgkmcnt(0)
	v_fmamk_f32 v38, v38, 0x3e38aa3b, v86
	v_fmac_f32_e32 v87, 0x3e38aa3b, v39
	v_add_u32_e32 v39, 35, v2
	v_cndmask_b32_e32 v38, v44, v38, vcc
	v_cmp_gt_u32_e32 vcc, s33, v39
	s_nop 1
	v_cndmask_b32_e32 v39, v44, v87, vcc
	ds_read2_b32 v[86:87], v84 offset0:48 offset1:49
	v_cmp_gt_u32_e32 vcc, s33, v85
	v_add_u32_e32 v85, 50, v2
	v_max3_f32 v47, v47, v38, v39
	s_waitcnt lgkmcnt(0)
	v_fmamk_f32 v32, v32, 0x3e38aa3b, v86
	v_fmac_f32_e32 v87, 0x3e38aa3b, v33
	v_add_u32_e32 v33, 49, v2
	v_cndmask_b32_e32 v32, v44, v32, vcc
	v_cmp_gt_u32_e32 vcc, s33, v33
	s_nop 1
	v_cndmask_b32_e32 v33, v44, v87, vcc
	ds_read2_b32 v[86:87], v84 offset0:50 offset1:51
	v_cmp_gt_u32_e32 vcc, s33, v85
	v_add_u32_e32 v85, 64, v2
	v_max3_f32 v47, v47, v32, v33
	s_waitcnt lgkmcnt(0)
	v_fmamk_f32 v34, v34, 0x3e38aa3b, v86
	v_fmac_f32_e32 v87, 0x3e38aa3b, v35
	v_add_u32_e32 v35, 51, v2
	v_cndmask_b32_e32 v34, v44, v34, vcc
	v_cmp_gt_u32_e32 vcc, s33, v35
	s_nop 1
	v_cndmask_b32_e32 v35, v44, v87, vcc
	ds_read2_b32 v[86:87], v84 offset0:64 offset1:65
	v_cmp_gt_u32_e32 vcc, s33, v85
	v_max3_f32 v47, v47, v34, v35
	s_waitcnt lgkmcnt(0)
	v_fmamk_f32 v28, v28, 0x3e38aa3b, v86
	v_fmac_f32_e32 v87, 0x3e38aa3b, v29
	v_add_u32_e32 v29, 0x41, v2
	v_cndmask_b32_e32 v28, v44, v28, vcc
	v_cmp_gt_u32_e32 vcc, s33, v29
	s_nop 1
	v_cndmask_b32_e32 v29, v44, v87, vcc
	ds_read2_b32 v[86:87], v84 offset0:66 offset1:67
	v_max3_f32 v85, v47, v28, v29
	v_add_u32_e32 v47, 0x42, v2
	v_cmp_gt_u32_e32 vcc, s33, v47
	s_waitcnt lgkmcnt(0)
	v_fmamk_f32 v30, v30, 0x3e38aa3b, v86
	v_cndmask_b32_e32 v47, v44, v30, vcc
	v_add_u32_e32 v30, 0x43, v2
	v_fmac_f32_e32 v87, 0x3e38aa3b, v31
	v_cmp_gt_u32_e32 vcc, s33, v30
	s_nop 1
	v_cndmask_b32_e32 v31, v44, v87, vcc
	ds_read2_b32 v[86:87], v84 offset0:80 offset1:81
	v_max3_f32 v30, v85, v47, v31
	v_add_u32_e32 v85, 0x50, v2
	v_cmp_gt_u32_e32 vcc, s33, v85
	v_add_u32_e32 v85, 0x52, v2
	s_waitcnt lgkmcnt(0)
	v_fmamk_f32 v24, v24, 0x3e38aa3b, v86
	v_fmac_f32_e32 v87, 0x3e38aa3b, v25
	v_add_u32_e32 v25, 0x51, v2
	v_cndmask_b32_e32 v24, v44, v24, vcc
	v_cmp_gt_u32_e32 vcc, s33, v25
	s_nop 1
	v_cndmask_b32_e32 v25, v44, v87, vcc
	ds_read2_b32 v[86:87], v84 offset0:82 offset1:83
	v_cmp_gt_u32_e32 vcc, s33, v85
	v_max3_f32 v30, v30, v24, v25
	s_waitcnt lgkmcnt(0)
	v_fmamk_f32 v26, v26, 0x3e38aa3b, v86
	v_cndmask_b32_e32 v85, v44, v26, vcc
	v_add_u32_e32 v26, 0x53, v2
	v_fmac_f32_e32 v87, 0x3e38aa3b, v27
	v_cmp_gt_u32_e32 vcc, s33, v26
	ds_read2_b32 v[26:27], v84 offset0:96 offset1:97
	s_waitcnt lgkmcnt(0)
	v_fmamk_f32 v20, v20, 0x3e38aa3b, v26
	v_add_u32_e32 v26, 0x60, v2
	v_cndmask_b32_e32 v86, v44, v87, vcc
	v_cmp_gt_u32_e32 vcc, s33, v26
	v_fmac_f32_e32 v27, 0x3e38aa3b, v21
	v_max3_f32 v30, v30, v85, v86
	v_cndmask_b32_e32 v26, v44, v20, vcc
	v_add_u32_e32 v20, 0x61, v2
	v_cmp_gt_u32_e32 vcc, s33, v20
	ds_read2_b32 v[20:21], v84 offset0:98 offset1:99
	s_waitcnt lgkmcnt(0)
	v_fmamk_f32 v20, v22, 0x3e38aa3b, v20
	v_add_u32_e32 v22, 0x62, v2
	v_cndmask_b32_e32 v27, v44, v27, vcc
	v_cmp_gt_u32_e32 vcc, s33, v22
	v_fmac_f32_e32 v21, 0x3e38aa3b, v23
	v_max3_f32 v30, v30, v26, v27
	v_cndmask_b32_e32 v87, v44, v20, vcc
	v_add_u32_e32 v20, 0x63, v2
	v_cmp_gt_u32_e32 vcc, s33, v20
	s_nop 1
	v_cndmask_b32_e32 v88, v44, v21, vcc
	ds_read2_b32 v[20:21], v84 offset0:112 offset1:113
	v_max3_f32 v22, v30, v87, v88
	s_waitcnt lgkmcnt(0)
	v_fmamk_f32 v16, v16, 0x3e38aa3b, v20
	v_add_u32_e32 v20, 0x70, v2
	v_cmp_gt_u32_e32 vcc, s33, v20
	v_fmac_f32_e32 v21, 0x3e38aa3b, v17
	s_nop 0
	v_cndmask_b32_e32 v89, v44, v16, vcc
	v_add_u32_e32 v16, 0x71, v2
	v_cmp_gt_u32_e32 vcc, s33, v16
	ds_read2_b32 v[16:17], v84 offset0:114 offset1:115
	s_waitcnt lgkmcnt(0)
; __device__ __forceinline__ void attn_group_mfma5(const bf16* QK, const float* bias2g, int ldil, int first, bf16* OACC, float* LSE, LAS unsigned char* lds, const int tid, const int bid, const int G) {
;     ...
;                 float sv = S[kb][e] * SC + tb[krel]; sv = ((unsigned)(kt0 + krel) >= (unsigned)Ls) ? NEGBIG : sv; S[kb][e] = sv; mx = fmaxf(mx, sv); }
;         mx = fmaxf(mx, swz_xor<16>(mx)); mx = fmaxf(mx, get_xor32(mx, lane));
;         float l = 0.f; v4u pb[5];
; #pragma unroll
;         for (int kb = 0; kb < 9; ++kb) {
;             const float p0 = __builtin_amdgcn_exp2f(S[kb][0] - mx), p1 = __builtin_amdgcn_exp2f(S[kb][1] - mx), p2 = __builtin_amdgcn_exp2f(S[kb][2] - mx), p3 = __builtin_amdgcn_exp2f(S[kb][3] - mx);
;             l += (p0 + p1) + (p2 + p3);
;             if (kb & 1) { pb[kb >> 1].z = cvtpk(p0, p1); pb[kb >> 1].w = cvtpk(p2, p3); } else { pb[kb >> 1].x = cvtpk(p0, p1); pb[kb >> 1].y = cvtpk(p2, p3); } }
;         pb[4].z = 0u; pb[4].w = 0u;
;         l += swz_xor<16>(l); l += get_xor32(l, lane);
;         f32x4 O[4];
; #pragma unroll
;         for (int db = 0; db < 4; ++db) O[db] = (f32x4){0.f, 0.f, 0.f, 0.f};
;         { const int vf = (2 * kq + (n >> 3)) & 7;
;           const unsigned vb0 = (unsigned)(size_t)(Vl + (16 * wq + 4 * kq + (n >> 2)) * 128 + 8 * (n & 1));
;           unsigned ad[4];
; #pragma unroll
;           for (int db = 0; db < 4; ++db) ad[db] = vb0 + (unsigned)(((2 * db + ((n & 3) >> 1)) ^ vf) * 16);
; #pragma unroll
;           for (int t = 0; t < 5; ++t) {
;               v2u l0, l1, l2, l3, h0 = (v2u){0u, 0u}, h1 = h0, h2 = h0, h3 = h0;
;               if (t < 4) asm volatile("ds_read_b64_tr_b16 %0, %8 offset:%12\n\tds_read_b64_tr_b16 %1, %9 offset:%12\n\tds_read_b64_tr_b16 %2, %10 offset:%12\n\tds_read_b64_tr_b16 %3, %11 offset:%12\n\t"
;                                       "ds_read_b64_tr_b16 %4, %8 offset:%13\n\tds_read_b64_tr_b16 %5, %9 offset:%13\n\tds_read_b64_tr_b16 %6, %10 offset:%13\n\tds_read_b64_tr_b16 %7, %11 offset:%13\n\ts_waitcnt lgkmcnt(0)"
;                                       : "=&v"(l0), "=&v"(l1), "=&v"(l2), "=&v"(l3), "=&v"(h0), "=&v"(h1), "=&v"(h2), "=&v"(h3) : "v"(ad[0]), "v"(ad[1]), "v"(ad[2]), "v"(ad[3]), "n"(t * 4096), "n"(t * 4096 + 2048) : "memory");
	v_fmamk_f32 v16, v18, 0x3e38aa3b, v16
	v_add_u32_e32 v18, 0x72, v2
	v_cndmask_b32_e32 v90, v44, v21, vcc
	v_cmp_gt_u32_e32 vcc, s33, v18
	v_fmac_f32_e32 v17, 0x3e38aa3b, v19
	v_max3_f32 v20, v22, v89, v90
	v_cndmask_b32_e32 v91, v44, v16, vcc
	v_add_u32_e32 v16, 0x73, v2
	v_cmp_gt_u32_e32 vcc, s33, v16
	s_nop 1
	v_cndmask_b32_e32 v92, v44, v17, vcc
	ds_read2_b32 v[16:17], v84 offset0:128 offset1:129
	v_max3_f32 v18, v20, v91, v92
	s_waitcnt lgkmcnt(0)
	v_fmamk_f32 v12, v12, 0x3e38aa3b, v16
	v_add_u32_e32 v16, 0x80, v2
	v_cmp_gt_u32_e32 vcc, s33, v16
	v_fmac_f32_e32 v17, 0x3e38aa3b, v13
	s_nop 0
	v_cndmask_b32_e32 v93, v44, v12, vcc
	v_add_u32_e32 v12, 0x81, v2
	v_cmp_gt_u32_e32 vcc, s33, v12
	ds_read2_b32 v[12:13], v84 offset0:130 offset1:131
	s_waitcnt lgkmcnt(0)
	v_fmamk_f32 v12, v14, 0x3e38aa3b, v12
	v_add_u32_e32 v14, 0x82, v2
	v_cndmask_b32_e32 v94, v44, v17, vcc
	v_cmp_gt_u32_e32 vcc, s33, v14
	v_add_u32_e32 v2, 0x83, v2
	v_fmac_f32_e32 v13, 0x3e38aa3b, v15
	v_cndmask_b32_e32 v84, v44, v12, vcc
	v_cmp_gt_u32_e32 vcc, s33, v2
	v_max3_f32 v16, v18, v93, v94
	s_nop 0
	v_cndmask_b32_e32 v44, v44, v13, vcc
	v_max3_f32 v2, v16, v84, v44
	v_mov_b32_e32 v12, v2
	s_nop 1
	v_permlane16_swap_b32_e32 v12, v2
	s_and_b64 vcc, exec, s[8:9]
	s_waitcnt lgkmcnt(0)
	v_max_f32_e32 v12, v12, v12
	v_max_f32_e32 v2, v2, v12
	v_mov_b32_e32 v12, v2
	s_nop 1
	v_permlane32_swap_b32_e32 v12, v2
	s_waitcnt lgkmcnt(0)
	v_max_f32_e32 v12, v12, v12
	v_max_f32_e32 v30, v2, v12
	v_sub_f32_e32 v1, v1, v30
	v_sub_f32_e32 v0, v0, v30
	v_exp_f32_e32 v12, v1
	v_sub_f32_e32 v1, v45, v30
	v_sub_f32_e32 v2, v46, v30
	v_exp_f32_e32 v0, v0
	v_exp_f32_e32 v1, v1
	v_exp_f32_e32 v13, v2
	s_nop 0
	v_pk_add_f32 v[14:15], v[0:1], v[12:13]
	v_cvt_pk_bf16_f32 v13, v1, v13
	v_sub_f32_e32 v1, v41, v30
	v_cvt_pk_bf16_f32 v12, v0, v12
	v_sub_f32_e32 v0, v40, v30
	v_exp_f32_e32 v2, v1
	v_sub_f32_e32 v1, v42, v30
	v_pk_add_f32 v[18:19], v[14:15], v[14:15] op_sel_hi:[0,1]
	v_exp_f32_e32 v0, v0
	v_exp_f32_e32 v15, v1
	v_sub_f32_e32 v1, v43, v30
	v_exp_f32_e32 v16, v1
	v_add_f32_e32 v1, v0, v2
	v_cvt_pk_bf16_f32 v14, v0, v2
	v_sub_f32_e32 v2, v37, v30
	v_add_f32_e32 v17, v15, v16
	v_cvt_pk_bf16_f32 v15, v15, v16
	v_sub_f32_e32 v0, v36, v30
	v_exp_f32_e32 v16, v2
	v_sub_f32_e32 v2, v38, v30
	v_exp_f32_e32 v0, v0
	v_exp_f32_e32 v18, v2
	v_sub_f32_e32 v2, v39, v30
	v_exp_f32_e32 v2, v2
	v_pk_add_f32 v[20:21], v[0:1], v[16:17]
	v_sub_f32_e32 v1, v33, v30
	v_cvt_pk_bf16_f32 v16, v0, v16
	v_pk_add_f32 v[22:23], v[18:19], v[2:3]
	v_cvt_pk_bf16_f32 v17, v18, v2
	v_sub_f32_e32 v0, v32, v30
	v_exp_f32_e32 v18, v1
	v_sub_f32_e32 v1, v34, v30
	v_sub_f32_e32 v2, v35, v30
	v_exp_f32_e32 v0, v0
	v_exp_f32_e32 v1, v1
	v_exp_f32_e32 v19, v2
	v_pk_add_f32 v[20:21], v[20:21], v[22:23]
	s_nop 0
	v_pk_add_f32 v[36:37], v[20:21], v[20:21] op_sel_hi:[0,1]
	v_pk_add_f32 v[20:21], v[0:1], v[18:19]
	v_cvt_pk_bf16_f32 v19, v1, v19
	v_sub_f32_e32 v1, v29, v30
	v_cvt_pk_bf16_f32 v18, v0, v18
	v_sub_f32_e32 v0, v28, v30
	v_exp_f32_e32 v2, v1
	v_sub_f32_e32 v1, v47, v30
	v_pk_add_f32 v[32:33], v[20:21], v[20:21] op_sel_hi:[0,1]
	v_exp_f32_e32 v0, v0
	v_exp_f32_e32 v21, v1
	v_sub_f32_e32 v1, v31, v30
	v_exp_f32_e32 v22, v1
	v_add_f32_e32 v1, v0, v2
	v_cvt_pk_bf16_f32 v20, v0, v2
	v_sub_f32_e32 v2, v25, v30
	v_add_f32_e32 v23, v21, v22
	v_cvt_pk_bf16_f32 v21, v21, v22
	v_exp_f32_e32 v22, v2
	v_sub_f32_e32 v2, v85, v30
	v_sub_f32_e32 v0, v24, v30
	v_exp_f32_e32 v32, v2
	v_sub_f32_e32 v2, v86, v30
	v_exp_f32_e32 v0, v0
	v_exp_f32_e32 v36, v2
	v_sub_f32_e32 v2, v88, v30
	v_add_u32_e32 v31, s1, v76
	v_pk_add_f32 v[24:25], v[0:1], v[22:23]
	v_pk_add_f32 v[28:29], v[32:33], v[36:37]
	v_sub_f32_e32 v1, v27, v30
	v_pk_add_f32 v[24:25], v[24:25], v[28:29]
	v_cvt_pk_bf16_f32 v22, v0, v22
	v_pk_add_f32 v[28:29], v[24:25], v[24:25] op_sel_hi:[0,1]
	v_sub_f32_e32 v0, v26, v30
	v_exp_f32_e32 v24, v1
	v_sub_f32_e32 v1, v87, v30
	v_exp_f32_e32 v0, v0
	v_exp_f32_e32 v1, v1
	v_exp_f32_e32 v25, v2
	v_cvt_pk_bf16_f32 v23, v32, v36
	s_mov_b32 s1, 0x8000
	v_add3_u32 v31, v31, v77, s1
	v_pk_add_f32 v[26:27], v[0:1], v[24:25]
	v_cvt_pk_bf16_f32 v24, v0, v24
	v_cvt_pk_bf16_f32 v25, v1, v25
	v_sub_f32_e32 v0, v89, v30
	v_sub_f32_e32 v1, v90, v30
	v_exp_f32_e32 v0, v0
	v_exp_f32_e32 v2, v1
	v_sub_f32_e32 v1, v91, v30
	v_pk_add_f32 v[32:33], v[26:27], v[26:27] op_sel_hi:[0,1]
	v_exp_f32_e32 v27, v1
	v_sub_f32_e32 v1, v92, v30
	v_exp_f32_e32 v28, v1
	v_add_f32_e32 v1, v0, v2
	v_cvt_pk_bf16_f32 v26, v0, v2
	v_sub_f32_e32 v2, v94, v30
	v_exp_f32_e32 v34, v2
	v_sub_f32_e32 v2, v84, v30
	v_sub_f32_e32 v0, v93, v30
	v_exp_f32_e32 v32, v2
	v_sub_f32_e32 v2, v44, v30
	v_add_f32_e32 v35, v27, v28
	v_cvt_pk_bf16_f32 v27, v27, v28
	v_exp_f32_e32 v0, v0
	v_exp_f32_e32 v28, v2
	v_add_u32_e32 v96, v80, v31
	v_add_u32_e32 v97, v81, v31
	v_pk_add_f32 v[36:37], v[0:1], v[34:35]
	v_pk_add_f32 v[38:39], v[32:33], v[28:29]
	v_cvt_pk_bf16_f32 v0, v0, v34
	v_pk_add_f32 v[36:37], v[36:37], v[38:39]
	v_cvt_pk_bf16_f32 v1, v32, v28
	v_add_f32_e32 v29, v36, v37
	v_add_u32_e32 v98, v82, v31
	v_add_u32_e32 v31, v83, v31
	ds_read_b64_tr_b16 v[44:45], v96 offset:0
	ds_read_b64_tr_b16 v[40:41], v97 offset:0
	ds_read_b64_tr_b16 v[36:37], v98 offset:0
	ds_read_b64_tr_b16 v[32:33], v31 offset:0
	ds_read_b64_tr_b16 v[46:47], v96 offset:0x800
	ds_read_b64_tr_b16 v[42:43], v97 offset:0x800
	ds_read_b64_tr_b16 v[38:39], v98 offset:0x800
	ds_read_b64_tr_b16 v[34:35], v31 offset:0x800
	s_waitcnt lgkmcnt(0)
; __device__ __forceinline__ void attn_group_mfma5(const bf16* QK, const float* bias2g, int ldil, int first, bf16* OACC, float* LSE, LAS unsigned char* lds, const int tid, const int bid, const int G) {
;     ...
;         l += swz_xor<16>(l); l += get_xor32(l, lane);
;         f32x4 O[4];
; #pragma unroll
;         for (int db = 0; db < 4; ++db) O[db] = (f32x4){0.f, 0.f, 0.f, 0.f};
;         { const int vf = (2 * kq + (n >> 3)) & 7;
;           const unsigned vb0 = (unsigned)(size_t)(Vl + (16 * wq + 4 * kq + (n >> 2)) * 128 + 8 * (n & 1));
;           unsigned ad[4];
; #pragma unroll
;           for (int db = 0; db < 4; ++db) ad[db] = vb0 + (unsigned)(((2 * db + ((n & 3) >> 1)) ^ vf) * 16);
; #pragma unroll
;           for (int t = 0; t < 5; ++t) {
;               v2u l0, l1, l2, l3, h0 = (v2u){0u, 0u}, h1 = h0, h2 = h0, h3 = h0;
;               if (t < 4) asm volatile("ds_read_b64_tr_b16 %0, %8 offset:%12\n\tds_read_b64_tr_b16 %1, %9 offset:%12\n\tds_read_b64_tr_b16 %2, %10 offset:%12\n\tds_read_b64_tr_b16 %3, %11 offset:%12\n\t"
;                                       "ds_read_b64_tr_b16 %4, %8 offset:%13\n\tds_read_b64_tr_b16 %5, %9 offset:%13\n\tds_read_b64_tr_b16 %6, %10 offset:%13\n\tds_read_b64_tr_b16 %7, %11 offset:%13\n\ts_waitcnt lgkmcnt(0)"
;                                       : "=&v"(l0), "=&v"(l1), "=&v"(l2), "=&v"(l3), "=&v"(h0), "=&v"(h1), "=&v"(h2), "=&v"(h3) : "v"(ad[0]), "v"(ad[1]), "v"(ad[2]), "v"(ad[3]), "n"(t * 4096), "n"(t * 4096 + 2048) : "memory");
;               else asm volatile("ds_read_b64_tr_b16 %0, %4 offset:%8\n\tds_read_b64_tr_b16 %1, %5 offset:%8\n\tds_read_b64_tr_b16 %2, %6 offset:%8\n\tds_read_b64_tr_b16 %3, %7 offset:%8\n\ts_waitcnt lgkmcnt(0)"
;                                 : "=&v"(l0), "=&v"(l1), "=&v"(l2), "=&v"(l3) : "v"(ad[0]), "v"(ad[1]), "v"(ad[2]), "v"(ad[3]), "n"(t * 4096) : "memory");
;               const bf16x8s pf = __builtin_bit_cast(bf16x8s, pb[t]);
;               O[0] = __builtin_amdgcn_mfma_f32_16x16x32_bf16(__builtin_bit_cast(bf16x8s, ((v4u){l0.x, l0.y, h0.x, h0.y})), pf, O[0], 0, 0, 0);
;               O[1] = __builtin_amdgcn_mfma_f32_16x16x32_bf16(__builtin_bit_cast(bf16x8s, ((v4u){l1.x, l1.y, h1.x, h1.y})), pf, O[1], 0, 0, 0);
;               O[2] = __builtin_amdgcn_mfma_f32_16x16x32_bf16(__builtin_bit_cast(bf16x8s, ((v4u){l2.x, l2.y, h2.x, h2.y})), pf, O[2], 0, 0, 0);
	v_mov_b32_e32 v2, v3
	v_mfma_f32_16x16x32_bf16 v[36:39], v[36:39], v[12:15], 0
	v_mov_b32_e32 v28, v29
	s_nop 1
	v_permlane16_swap_b32_e32 v28, v29
	s_waitcnt lgkmcnt(0)
	v_add_f32_e32 v28, v29, v28
	v_mfma_f32_16x16x32_bf16 v[44:47], v[44:47], v[12:15], 0
	v_mov_b32_e32 v29, v28
	s_nop 1
	v_permlane32_swap_b32_e32 v29, v28
	v_mfma_f32_16x16x32_bf16 v[40:43], v[40:43], v[12:15], 0
	v_mfma_f32_16x16x32_bf16 v[12:15], v[32:35], v[12:15], 0
	ds_read_b64_tr_b16 v[92:93], v96 offset:0x1000
	ds_read_b64_tr_b16 v[88:89], v97 offset:0x1000
	ds_read_b64_tr_b16 v[84:85], v98 offset:0x1000
	ds_read_b64_tr_b16 v[32:33], v31 offset:0x1000
	ds_read_b64_tr_b16 v[94:95], v96 offset:0x1800
	ds_read_b64_tr_b16 v[90:91], v97 offset:0x1800
	ds_read_b64_tr_b16 v[86:87], v98 offset:0x1800
	ds_read_b64_tr_b16 v[34:35], v31 offset:0x1800
	s_waitcnt lgkmcnt(0)
	s_nop 0
	v_mfma_f32_16x16x32_bf16 v[36:39], v[84:87], v[16:19], v[36:39]
	v_mfma_f32_16x16x32_bf16 v[44:47], v[92:95], v[16:19], v[44:47]
	v_mfma_f32_16x16x32_bf16 v[40:43], v[88:91], v[16:19], v[40:43]
	v_mfma_f32_16x16x32_bf16 v[12:15], v[32:35], v[16:19], v[12:15]
	ds_read_b64_tr_b16 v[88:89], v96 offset:0x2000
	ds_read_b64_tr_b16 v[84:85], v97 offset:0x2000
	ds_read_b64_tr_b16 v[32:33], v98 offset:0x2000
	ds_read_b64_tr_b16 v[16:17], v31 offset:0x2000
	ds_read_b64_tr_b16 v[90:91], v96 offset:0x2800
	ds_read_b64_tr_b16 v[86:87], v97 offset:0x2800
	ds_read_b64_tr_b16 v[34:35], v98 offset:0x2800
	ds_read_b64_tr_b16 v[18:19], v31 offset:0x2800
	s_waitcnt lgkmcnt(0)
	s_nop 0
	v_mfma_f32_16x16x32_bf16 v[32:35], v[32:35], v[20:23], v[36:39]
	v_mfma_f32_16x16x32_bf16 v[44:47], v[88:91], v[20:23], v[44:47]
	v_mfma_f32_16x16x32_bf16 v[40:43], v[84:87], v[20:23], v[40:43]
	v_mfma_f32_16x16x32_bf16 v[12:15], v[16:19], v[20:23], v[12:15]
	ds_read_b64_tr_b16 v[84:85], v96 offset:0x3000
	ds_read_b64_tr_b16 v[36:37], v97 offset:0x3000
	ds_read_b64_tr_b16 v[20:21], v98 offset:0x3000
	ds_read_b64_tr_b16 v[16:17], v31 offset:0x3000
	ds_read_b64_tr_b16 v[86:87], v96 offset:0x3800
	ds_read_b64_tr_b16 v[38:39], v97 offset:0x3800
	ds_read_b64_tr_b16 v[22:23], v98 offset:0x3800
	ds_read_b64_tr_b16 v[18:19], v31 offset:0x3800
	s_waitcnt lgkmcnt(0)
	s_nop 0
	v_mfma_f32_16x16x32_bf16 v[32:35], v[20:23], v[24:27], v[32:35]
	v_mov_b32_e32 v22, v3
	v_mov_b32_e32 v23, v3
	v_mfma_f32_16x16x32_bf16 v[44:47], v[84:87], v[24:27], v[44:47]
	v_mfma_f32_16x16x32_bf16 v[36:39], v[36:39], v[24:27], v[40:43]
	v_mfma_f32_16x16x32_bf16 v[12:15], v[16:19], v[24:27], v[12:15]
	ds_read_b64_tr_b16 v[20:21], v96 offset:0x4000
	ds_read_b64_tr_b16 v[18:19], v97 offset:0x4000
	ds_read_b64_tr_b16 v[16:17], v98 offset:0x4000
	ds_read_b64_tr_b16 v[40:41], v31 offset:0x4000
	s_waitcnt lgkmcnt(0)
	s_nop 1
	v_mov_b32_e32 v42, v3
	v_mov_b32_e32 v43, v3
	v_mfma_f32_16x16x32_bf16 v[24:27], v[20:23], v[0:3], v[44:47]
	v_mov_b32_e32 v20, v3
	v_mov_b32_e32 v21, v3
	v_mfma_f32_16x16x32_bf16 v[12:15], v[40:43], v[0:3], v[12:15]
	s_nop 0
	v_mfma_f32_16x16x32_bf16 v[20:23], v[18:21], v[0:3], v[36:39]
	v_mov_b32_e32 v18, v3
	v_mov_b32_e32 v19, v3
	s_nop 1
	v_mfma_f32_16x16x32_bf16 v[16:19], v[16:19], v[0:3], v[32:35]
	s_waitcnt lgkmcnt(0)
	v_add_f32_e32 v1, v28, v29
	v_rcp_f32_e32 v0, v1
	v_log_f32_e32 v1, v1
	s_nop 0
	v_add_f32_e32 v28, v30, v1
	s_cbranch_vccnz .LBB0_223
	v_max_f32_e32 v1, v28, v28
	s_waitcnt vmcnt(0)
	v_max_f32_e32 v2, v59, v59
	v_max_f32_e32 v2, v2, v1
	v_sub_f32_e32 v1, v59, v2
	v_sub_f32_e32 v28, v28, v2
	v_exp_f32_e32 v1, v1
	v_exp_f32_e32 v28, v28
	s_nop 0
	v_add_f32_e32 v30, v1, v28
	v_rcp_f32_e32 v29, v30
	v_log_f32_e32 v30, v30
	v_mul_f32_e32 v28, v28, v29
	v_pk_mul_f32 v[0:1], v[0:1], v[28:29]
	v_add_f32_e32 v28, v2, v30
	v_mov_b32_e32 v2, v1
	s_and_saveexec_b64 s[8:9], s[4:5]
	s_cbranch_execz .LBB0_221

; #define LAS __attribute__((address_space(3)))
; __device__ __forceinline__ void attn_group_ring(const bf16* QK, const float* bias2g, int ldil, int first, bf16* OACC, float* LSE, LAS unsigned char* lds, const int tid, const int bid, const int G) {
;     ...
;         const LAS float* tb = tab + (32 + 4 * kq - n);
;         int kt0 = q4 * 128 - 64 + 16 * wq + 4 * kq; asm volatile("" : "+v"(kt0));
;         float mx = NEGBIG;
; #pragma unroll
;         for (int kb = 0; kb < 9; ++kb)
; #pragma unroll
;             for (int e = 0; e < 4; ++e) { const int krel = 16 * kb + e;
;                 float sv = S[kb][e] * SC + tb[krel]; sv = ((unsigned)(kt0 + krel) >= (unsigned)Ls) ? NEGBIG : sv; S[kb][e] = sv; mx = fmaxf(mx, sv); }
;     ...
;           for (int t = 0; t < 5; ++t) {
;               const int wlo = 16 * wq + 32 * t, whi = wlo + 16;
;               const unsigned blo = (unsigned)(size_t)(lds + ((a + (wlo >> 7)) & 3) * 32768 + 16384 + (wlo & 127) * 128), bhi = (unsigned)(size_t)(lds + ((a + (whi >> 7)) & 3) * 32768 + 16384 + (whi & 127) * 128);
.LBB0_243:
	s_movk_i32 s70, 0xff
	s_movk_i32 s71, 0xdf
	v_add_u32_e32 v2, s1, v83
	ds_read2_b32 v[0:1], v65 offset0:32 offset1:33
	ds_read2_b32 v[86:87], v65 offset0:34 offset1:35
	v_cmp_gt_u32_e32 vcc, s13, v2
	s_add_i32 s1, s78, s87
	s_add_i32 s1, s1, s0
	s_waitcnt lgkmcnt(0)
	v_fmamk_f32 v0, v44, 0x3e38aa3b, v0
	v_mov_b32_e32 v44, s12
	v_fmac_f32_e32 v1, 0x3e38aa3b, v45
	v_add_u32_e32 v45, 1, v2
	v_cndmask_b32_e32 v0, v44, v0, vcc
	v_cmp_gt_u32_e32 vcc, s13, v45
	v_fmamk_f32 v45, v46, 0x3e38aa3b, v86
	v_add_u32_e32 v46, 2, v2
	v_cndmask_b32_e32 v1, v44, v1, vcc
	v_cmp_gt_u32_e32 vcc, s13, v46
	v_add_u32_e32 v46, 3, v2
	v_fmac_f32_e32 v87, 0x3e38aa3b, v47
	v_cndmask_b32_e32 v45, v44, v45, vcc
	v_cmp_gt_u32_e32 vcc, s13, v46
	v_max3_f32 v85, s12, v0, v1
	s_lshl_b32 s1, s1, 15
	v_cndmask_b32_e32 v46, v44, v87, vcc
	ds_read2_b32 v[86:87], v65 offset0:48 offset1:49
	v_max3_f32 v47, v85, v45, v46
	v_add_u32_e32 v85, 16, v2
	v_cmp_gt_u32_e32 vcc, s13, v85
	v_add_u32_e32 v85, 18, v2
	s_waitcnt lgkmcnt(0)
	v_fmamk_f32 v40, v40, 0x3e38aa3b, v86
	v_fmac_f32_e32 v87, 0x3e38aa3b, v41
	v_add_u32_e32 v41, 17, v2
	v_cndmask_b32_e32 v40, v44, v40, vcc
	v_cmp_gt_u32_e32 vcc, s13, v41
	s_and_b32 s1, s1, 0x18000
	s_add_i32 s1, s93, s1
	v_cndmask_b32_e32 v41, v44, v87, vcc
	ds_read2_b32 v[86:87], v65 offset0:50 offset1:51
	v_cmp_gt_u32_e32 vcc, s13, v85
	v_add_u32_e32 v85, 32, v2
	v_max3_f32 v47, v47, v40, v41
	s_addk_i32 s1, 0x4000
	s_waitcnt lgkmcnt(0)
	v_fmamk_f32 v42, v42, 0x3e38aa3b, v86
	v_fmac_f32_e32 v87, 0x3e38aa3b, v43
	v_add_u32_e32 v43, 19, v2
	v_cndmask_b32_e32 v42, v44, v42, vcc
	v_cmp_gt_u32_e32 vcc, s13, v43
	s_nop 1
	v_cndmask_b32_e32 v43, v44, v87, vcc
	ds_read2_b32 v[86:87], v65 offset0:64 offset1:65
	v_cmp_gt_u32_e32 vcc, s13, v85
	v_add_u32_e32 v85, 34, v2
	v_max3_f32 v47, v47, v42, v43
	s_waitcnt lgkmcnt(0)
	v_fmamk_f32 v36, v36, 0x3e38aa3b, v86
	v_fmac_f32_e32 v87, 0x3e38aa3b, v37
	v_add_u32_e32 v37, 33, v2
	v_cndmask_b32_e32 v36, v44, v36, vcc
	v_cmp_gt_u32_e32 vcc, s13, v37
	s_nop 1
	v_cndmask_b32_e32 v37, v44, v87, vcc
	ds_read2_b32 v[86:87], v65 offset0:66 offset1:67
	v_cmp_gt_u32_e32 vcc, s13, v85
	v_add_u32_e32 v85, 48, v2
	v_max3_f32 v47, v47, v36, v37
	s_waitcnt lgkmcnt(0)
	v_fmamk_f32 v38, v38, 0x3e38aa3b, v86
	v_fmac_f32_e32 v87, 0x3e38aa3b, v39
	v_add_u32_e32 v39, 35, v2
	v_cndmask_b32_e32 v38, v44, v38, vcc
	v_cmp_gt_u32_e32 vcc, s13, v39
	s_nop 1
	v_cndmask_b32_e32 v39, v44, v87, vcc
	ds_read2_b32 v[86:87], v65 offset0:80 offset1:81
	v_cmp_gt_u32_e32 vcc, s13, v85
	v_max3_f32 v47, v47, v38, v39
	s_waitcnt lgkmcnt(0)
	v_fmamk_f32 v32, v32, 0x3e38aa3b, v86
	v_fmac_f32_e32 v87, 0x3e38aa3b, v33
	v_add_u32_e32 v33, 49, v2
	v_cndmask_b32_e32 v32, v44, v32, vcc
	v_cmp_gt_u32_e32 vcc, s13, v33
	s_nop 1
	v_cndmask_b32_e32 v33, v44, v87, vcc
	ds_read2_b32 v[86:87], v65 offset0:82 offset1:83
	v_max3_f32 v85, v47, v32, v33
	v_add_u32_e32 v47, 50, v2
	v_cmp_gt_u32_e32 vcc, s13, v47
	s_waitcnt lgkmcnt(0)
	v_fmamk_f32 v34, v34, 0x3e38aa3b, v86
	v_cndmask_b32_e32 v47, v44, v34, vcc
	v_add_u32_e32 v34, 51, v2
	v_fmac_f32_e32 v87, 0x3e38aa3b, v35
	v_cmp_gt_u32_e32 vcc, s13, v34
	v_add_u32_e32 v34, 64, v2
	s_nop 0
	v_cndmask_b32_e32 v35, v44, v87, vcc
	ds_read2_b32 v[86:87], v65 offset0:96 offset1:97
	v_cmp_gt_u32_e32 vcc, s13, v34
	v_max3_f32 v85, v85, v47, v35
	s_waitcnt lgkmcnt(0)
	v_fmamk_f32 v28, v28, 0x3e38aa3b, v86
	v_cndmask_b32_e32 v34, v44, v28, vcc
	v_add_u32_e32 v28, 0x41, v2
	v_fmac_f32_e32 v87, 0x3e38aa3b, v29
	v_cmp_gt_u32_e32 vcc, s13, v28
	s_nop 1
	v_cndmask_b32_e32 v29, v44, v87, vcc
	ds_read2_b32 v[86:87], v65 offset0:98 offset1:99
	v_max3_f32 v28, v85, v34, v29
	v_add_u32_e32 v85, 0x42, v2
	v_cmp_gt_u32_e32 vcc, s13, v85
	v_add_u32_e32 v85, 0x50, v2
	s_waitcnt lgkmcnt(0)
	v_fmamk_f32 v30, v30, 0x3e38aa3b, v86
	v_fmac_f32_e32 v87, 0x3e38aa3b, v31
	v_add_u32_e32 v31, 0x43, v2
	v_cndmask_b32_e32 v30, v44, v30, vcc
	v_cmp_gt_u32_e32 vcc, s13, v31
	s_nop 1
	v_cndmask_b32_e32 v31, v44, v87, vcc
	ds_read2_b32 v[86:87], v65 offset0:112 offset1:113
	v_cmp_gt_u32_e32 vcc, s13, v85
	v_max3_f32 v28, v28, v30, v31
	s_waitcnt lgkmcnt(0)
	v_fmamk_f32 v24, v24, 0x3e38aa3b, v86
	v_cndmask_b32_e32 v85, v44, v24, vcc
	v_add_u32_e32 v24, 0x51, v2
	v_fmac_f32_e32 v87, 0x3e38aa3b, v25
	v_cmp_gt_u32_e32 vcc, s13, v24
	ds_read2_b32 v[24:25], v65 offset0:114 offset1:115
	s_waitcnt lgkmcnt(0)
	v_fmamk_f32 v24, v26, 0x3e38aa3b, v24
	v_add_u32_e32 v26, 0x52, v2
	v_cndmask_b32_e32 v86, v44, v87, vcc
	v_cmp_gt_u32_e32 vcc, s13, v26
	v_fmac_f32_e32 v25, 0x3e38aa3b, v27
	v_max3_f32 v28, v28, v85, v86
	v_cndmask_b32_e32 v89, v44, v24, vcc
	v_add_u32_e32 v24, 0x53, v2
	v_cmp_gt_u32_e32 vcc, s13, v24
	s_nop 1
	v_cndmask_b32_e32 v90, v44, v25, vcc
	ds_read2_b32 v[24:25], v65 offset0:128 offset1:129
	v_max3_f32 v26, v28, v89, v90
	s_waitcnt lgkmcnt(0)
	v_fmamk_f32 v20, v20, 0x3e38aa3b, v24
	v_add_u32_e32 v24, 0x60, v2
	v_cmp_gt_u32_e32 vcc, s13, v24
	v_fmac_f32_e32 v25, 0x3e38aa3b, v21
	s_nop 0
	v_cndmask_b32_e32 v87, v44, v20, vcc
	v_add_u32_e32 v20, 0x61, v2
	v_cmp_gt_u32_e32 vcc, s13, v20
	ds_read2_b32 v[20:21], v65 offset0:130 offset1:131
	s_waitcnt lgkmcnt(0)
	v_fmamk_f32 v20, v22, 0x3e38aa3b, v20
	v_add_u32_e32 v22, 0x62, v2
	v_cndmask_b32_e32 v88, v44, v25, vcc
	v_cmp_gt_u32_e32 vcc, s13, v22
	v_fmac_f32_e32 v21, 0x3e38aa3b, v23
	v_max3_f32 v24, v26, v87, v88
	v_cndmask_b32_e32 v91, v44, v20, vcc
	v_add_u32_e32 v20, 0x63, v2
	v_cmp_gt_u32_e32 vcc, s13, v20
	s_nop 1
	v_cndmask_b32_e32 v92, v44, v21, vcc
	ds_read2_b32 v[20:21], v65 offset0:144 offset1:145
	v_max3_f32 v22, v24, v91, v92
	s_waitcnt lgkmcnt(0)
; __device__ __forceinline__ void attn_group_ring(const bf16* QK, const float* bias2g, int ldil, int first, bf16* OACC, float* LSE, LAS unsigned char* lds, const int tid, const int bid, const int G) {
;     ...
;                 float sv = S[kb][e] * SC + tb[krel]; sv = ((unsigned)(kt0 + krel) >= (unsigned)Ls) ? NEGBIG : sv; S[kb][e] = sv; mx = fmaxf(mx, sv); }
;         mx = fmaxf(mx, swz_xor<16>(mx)); mx = fmaxf(mx, get_xor32(mx, lane));
;         float l = 0.f; v4u pb[5];
; #pragma unroll
;         for (int kb = 0; kb < 9; ++kb) {
;             const float p0 = __builtin_amdgcn_exp2f(S[kb][0] - mx), p1 = __builtin_amdgcn_exp2f(S[kb][1] - mx), p2 = __builtin_amdgcn_exp2f(S[kb][2] - mx), p3 = __builtin_amdgcn_exp2f(S[kb][3] - mx);
;             l += (p0 + p1) + (p2 + p3);
;             if (kb & 1) { pb[kb >> 1].z = cvtpk(p0, p1); pb[kb >> 1].w = cvtpk(p2, p3); } else { pb[kb >> 1].x = cvtpk(p0, p1); pb[kb >> 1].y = cvtpk(p2, p3); } }
;         pb[4].z = 0u; pb[4].w = 0u;
;         l += swz_xor<16>(l); l += get_xor32(l, lane);
;         f32x4 O[4];
; #pragma unroll
;         for (int db = 0; db < 4; ++db) O[db] = (f32x4){0.f, 0.f, 0.f, 0.f};
;         { const int vf = (2 * kq + (n >> 3)) & 7;
;           unsigned pcs[4];
; #pragma unroll
;           for (int db = 0; db < 4; ++db) pcs[db] = (unsigned)((4 * kq + (n >> 2)) * 128 + 8 * (n & 1) + (((2 * db + ((n & 3) >> 1)) ^ vf) * 16));
; #pragma unroll
;           for (int t = 0; t < 5; ++t) {
;               const int wlo = 16 * wq + 32 * t, whi = wlo + 16;
;               const unsigned blo = (unsigned)(size_t)(lds + ((a + (wlo >> 7)) & 3) * 32768 + 16384 + (wlo & 127) * 128), bhi = (unsigned)(size_t)(lds + ((a + (whi >> 7)) & 3) * 32768 + 16384 + (whi & 127) * 128);
;               v2u l0, l1, l2, l3, h0 = (v2u){0u, 0u}, h1 = h0, h2 = h0, h3 = h0;
;               const unsigned a0 = blo + pcs[0], a1 = blo + pcs[1], a2 = blo + pcs[2], a3 = blo + pcs[3];
;               if (t < 4) { const unsigned c0 = bhi + pcs[0], c1 = bhi + pcs[1], c2 = bhi + pcs[2], c3 = bhi + pcs[3];
;                   asm volatile("ds_read_b64_tr_b16 %0, %8\n\tds_read_b64_tr_b16 %1, %9\n\tds_read_b64_tr_b16 %2, %10\n\tds_read_b64_tr_b16 %3, %11\n\t"
;                                "ds_read_b64_tr_b16 %4, %12\n\tds_read_b64_tr_b16 %5, %13\n\tds_read_b64_tr_b16 %6, %14\n\tds_read_b64_tr_b16 %7, %15\n\ts_waitcnt lgkmcnt(0)"
	v_fmamk_f32 v16, v16, 0x3e38aa3b, v20
	v_add_u32_e32 v20, 0x70, v2
	v_cmp_gt_u32_e32 vcc, s13, v20
	v_fmac_f32_e32 v21, 0x3e38aa3b, v17
	s_nop 0
	v_cndmask_b32_e32 v93, v44, v16, vcc
	v_add_u32_e32 v16, 0x71, v2
	v_cmp_gt_u32_e32 vcc, s13, v16
	ds_read2_b32 v[16:17], v65 offset0:146 offset1:147
	s_waitcnt lgkmcnt(0)
	v_fmamk_f32 v16, v18, 0x3e38aa3b, v16
	v_add_u32_e32 v18, 0x72, v2
	v_cndmask_b32_e32 v94, v44, v21, vcc
	v_cmp_gt_u32_e32 vcc, s13, v18
	v_fmac_f32_e32 v17, 0x3e38aa3b, v19
	v_max3_f32 v20, v22, v93, v94
	v_cndmask_b32_e32 v95, v44, v16, vcc
	v_add_u32_e32 v16, 0x73, v2
	v_cmp_gt_u32_e32 vcc, s13, v16
	s_nop 1
	v_cndmask_b32_e32 v96, v44, v17, vcc
	ds_read2_b32 v[16:17], v65 offset0:160 offset1:161
	v_max3_f32 v18, v20, v95, v96
	s_waitcnt lgkmcnt(0)
	v_fmamk_f32 v12, v12, 0x3e38aa3b, v16
	v_add_u32_e32 v16, 0x80, v2
	v_cmp_gt_u32_e32 vcc, s13, v16
	v_fmac_f32_e32 v17, 0x3e38aa3b, v13
	s_nop 0
	v_cndmask_b32_e32 v97, v44, v12, vcc
	v_add_u32_e32 v12, 0x81, v2
	v_cmp_gt_u32_e32 vcc, s13, v12
	ds_read2_b32 v[12:13], v65 offset0:162 offset1:163
	s_waitcnt lgkmcnt(0)
	v_fmamk_f32 v12, v14, 0x3e38aa3b, v12
	v_add_u32_e32 v14, 0x82, v2
	v_cndmask_b32_e32 v98, v44, v17, vcc
	v_cmp_gt_u32_e32 vcc, s13, v14
	v_add_u32_e32 v2, 0x83, v2
	v_fmac_f32_e32 v13, 0x3e38aa3b, v15
	v_cndmask_b32_e32 v99, v44, v12, vcc
	v_cmp_gt_u32_e32 vcc, s13, v2
	v_max3_f32 v16, v18, v97, v98
	s_nop 0
	v_cndmask_b32_e32 v44, v44, v13, vcc
	v_max3_f32 v2, v16, v99, v44
	v_mov_b32_e32 v12, v2
	s_nop 1
	v_permlane16_swap_b32_e32 v12, v2
	s_and_b64 vcc, exec, s[4:5]
	s_waitcnt lgkmcnt(0)
	v_max_f32_e32 v12, v12, v12
	v_max_f32_e32 v2, v2, v12
	v_mov_b32_e32 v12, v2
	s_nop 1
	v_permlane32_swap_b32_e32 v12, v2
	s_waitcnt lgkmcnt(0)
	v_max_f32_e32 v12, v12, v12
	v_max_f32_e32 v28, v2, v12
	v_sub_f32_e32 v1, v1, v28
	v_sub_f32_e32 v0, v0, v28
	v_exp_f32_e32 v12, v1
	v_sub_f32_e32 v1, v45, v28
	v_sub_f32_e32 v2, v46, v28
	v_exp_f32_e32 v0, v0
	v_exp_f32_e32 v1, v1
	v_exp_f32_e32 v13, v2
	v_cvt_pk_bf16_f32 v24, v0, v12
	v_pk_add_f32 v[14:15], v[0:1], v[12:13]
	v_cvt_pk_bf16_f32 v25, v1, v13
	v_sub_f32_e32 v1, v41, v28
	v_sub_f32_e32 v0, v40, v28
	v_exp_f32_e32 v2, v1
	v_sub_f32_e32 v1, v42, v28
	v_pk_add_f32 v[14:15], v[14:15], v[14:15] op_sel_hi:[0,1]
	v_exp_f32_e32 v0, v0
	v_exp_f32_e32 v12, v1
	v_sub_f32_e32 v1, v43, v28
	v_exp_f32_e32 v14, v1
	v_add_f32_e32 v1, v0, v2
	v_cvt_pk_bf16_f32 v26, v0, v2
	v_sub_f32_e32 v2, v37, v28
	v_add_f32_e32 v13, v12, v14
	v_cvt_pk_bf16_f32 v27, v12, v14
	v_sub_f32_e32 v0, v36, v28
	v_exp_f32_e32 v12, v2
	v_sub_f32_e32 v2, v38, v28
	v_exp_f32_e32 v0, v0
	v_exp_f32_e32 v14, v2
	v_sub_f32_e32 v2, v39, v28
	v_exp_f32_e32 v2, v2
	v_pk_add_f32 v[16:17], v[0:1], v[12:13]
	v_sub_f32_e32 v1, v33, v28
	v_cvt_pk_bf16_f32 v20, v0, v12
	v_pk_add_f32 v[18:19], v[14:15], v[2:3]
	v_cvt_pk_bf16_f32 v21, v14, v2
	v_sub_f32_e32 v0, v32, v28
	v_exp_f32_e32 v12, v1
	v_sub_f32_e32 v1, v47, v28
	v_sub_f32_e32 v2, v35, v28
	v_exp_f32_e32 v0, v0
	v_exp_f32_e32 v1, v1
	v_exp_f32_e32 v13, v2
	v_pk_add_f32 v[16:17], v[16:17], v[18:19]
	v_cvt_pk_bf16_f32 v22, v0, v12
	v_pk_add_f32 v[36:37], v[16:17], v[16:17] op_sel_hi:[0,1]
	v_pk_add_f32 v[14:15], v[0:1], v[12:13]
	v_cvt_pk_bf16_f32 v23, v1, v13
	v_sub_f32_e32 v1, v29, v28
	v_sub_f32_e32 v0, v34, v28
	v_exp_f32_e32 v2, v1
	v_sub_f32_e32 v1, v30, v28
	v_pk_add_f32 v[14:15], v[14:15], v[14:15] op_sel_hi:[0,1]
	v_exp_f32_e32 v0, v0
	v_exp_f32_e32 v12, v1
	v_sub_f32_e32 v1, v31, v28
	v_exp_f32_e32 v14, v1
	v_add_f32_e32 v1, v0, v2
	v_cvt_pk_bf16_f32 v16, v0, v2
	v_sub_f32_e32 v2, v86, v28
	v_add_f32_e32 v13, v12, v14
	v_cvt_pk_bf16_f32 v17, v12, v14
	v_exp_f32_e32 v12, v2
	v_sub_f32_e32 v2, v89, v28
	v_sub_f32_e32 v0, v85, v28
	v_exp_f32_e32 v14, v2
	v_sub_f32_e32 v2, v90, v28
	v_exp_f32_e32 v0, v0
	v_exp_f32_e32 v36, v2
	v_sub_f32_e32 v2, v92, v28
	v_add_u32_e32 v85, s1, v81
	v_pk_add_f32 v[18:19], v[0:1], v[12:13]
	v_pk_add_f32 v[30:31], v[14:15], v[36:37]
	v_sub_f32_e32 v1, v88, v28
	v_pk_add_f32 v[18:19], v[18:19], v[30:31]
	v_exp_f32_e32 v13, v2
	v_pk_add_f32 v[30:31], v[18:19], v[18:19] op_sel_hi:[0,1]
	v_cvt_pk_bf16_f32 v18, v0, v12
	v_sub_f32_e32 v0, v87, v28
	v_exp_f32_e32 v12, v1
	v_sub_f32_e32 v1, v91, v28
	v_exp_f32_e32 v0, v0
	v_exp_f32_e32 v1, v1
	v_cvt_pk_bf16_f32 v19, v14, v36
	v_add_u32_e32 v86, s1, v80
	v_add_u32_e32 v87, s1, v79
	v_pk_add_f32 v[14:15], v[0:1], v[12:13]
	v_cvt_pk_bf16_f32 v12, v0, v12
	v_cvt_pk_bf16_f32 v13, v1, v13
	v_sub_f32_e32 v0, v93, v28
	v_sub_f32_e32 v1, v94, v28
	v_exp_f32_e32 v0, v0
	v_exp_f32_e32 v2, v1
	v_sub_f32_e32 v1, v95, v28
	v_pk_add_f32 v[32:33], v[14:15], v[14:15] op_sel_hi:[0,1]
	v_exp_f32_e32 v15, v1
	v_sub_f32_e32 v1, v96, v28
	v_exp_f32_e32 v29, v1
	v_add_f32_e32 v1, v0, v2
	v_cvt_pk_bf16_f32 v14, v0, v2
	v_sub_f32_e32 v2, v98, v28
	v_exp_f32_e32 v34, v2
	v_sub_f32_e32 v2, v99, v28
	v_exp_f32_e32 v32, v2
	v_sub_f32_e32 v2, v44, v28
	v_exp_f32_e32 v30, v2
	v_sub_f32_e32 v0, v97, v28
	v_exp_f32_e32 v0, v0
	v_add_f32_e32 v35, v15, v29
	v_pk_add_f32 v[38:39], v[32:33], v[30:31]
	v_add_u32_e32 v31, s1, v82
	s_add_i32 s1, s79, s87
	s_add_i32 s1, s1, s0
	s_lshl_b32 s1, s1, 15
	s_and_b32 s1, s1, 0x18000
	s_add_i32 s1, s95, s1
	s_addk_i32 s1, 0x4000
	v_add_u32_e32 v88, s1, v79
	v_add_u32_e32 v89, s1, v80
	v_add_u32_e32 v90, s1, v81
	v_add_u32_e32 v91, s1, v82
	s_add_i32 s1, s82, s87
	s_add_i32 s1, s1, s0
	s_lshl_b32 s1, s1, 15
	s_and_b32 s1, s1, 0x18000
	v_pk_add_f32 v[36:37], v[0:1], v[34:35]
	s_add_i32 s1, s96, s1
	v_pk_add_f32 v[36:37], v[36:37], v[38:39]
	s_addk_i32 s1, 0x4000
	v_cvt_pk_bf16_f32 v15, v15, v29
	v_add_f32_e32 v29, v36, v37
	v_cvt_pk_bf16_f32 v0, v0, v34
	v_cvt_pk_bf16_f32 v1, v32, v30
	ds_read_b64_tr_b16 v[44:45], v87
	ds_read_b64_tr_b16 v[40:41], v86
	ds_read_b64_tr_b16 v[36:37], v85
	ds_read_b64_tr_b16 v[32:33], v31
	ds_read_b64_tr_b16 v[46:47], v88
	ds_read_b64_tr_b16 v[42:43], v89
	ds_read_b64_tr_b16 v[38:39], v90
	ds_read_b64_tr_b16 v[34:35], v91
	s_waitcnt lgkmcnt(0)
; __device__ __forceinline__ void attn_group_ring(const bf16* QK, const float* bias2g, int ldil, int first, bf16* OACC, float* LSE, LAS unsigned char* lds, const int tid, const int bid, const int G) {
;     ...
;         l += swz_xor<16>(l); l += get_xor32(l, lane);
;         f32x4 O[4];
; #pragma unroll
;         for (int db = 0; db < 4; ++db) O[db] = (f32x4){0.f, 0.f, 0.f, 0.f};
;         { const int vf = (2 * kq + (n >> 3)) & 7;
;           unsigned pcs[4];
; #pragma unroll
;           for (int db = 0; db < 4; ++db) pcs[db] = (unsigned)((4 * kq + (n >> 2)) * 128 + 8 * (n & 1) + (((2 * db + ((n & 3) >> 1)) ^ vf) * 16));
; #pragma unroll
;           for (int t = 0; t < 5; ++t) {
;               const int wlo = 16 * wq + 32 * t, whi = wlo + 16;
;               const unsigned blo = (unsigned)(size_t)(lds + ((a + (wlo >> 7)) & 3) * 32768 + 16384 + (wlo & 127) * 128), bhi = (unsigned)(size_t)(lds + ((a + (whi >> 7)) & 3) * 32768 + 16384 + (whi & 127) * 128);
;               v2u l0, l1, l2, l3, h0 = (v2u){0u, 0u}, h1 = h0, h2 = h0, h3 = h0;
;               const unsigned a0 = blo + pcs[0], a1 = blo + pcs[1], a2 = blo + pcs[2], a3 = blo + pcs[3];
;               if (t < 4) { const unsigned c0 = bhi + pcs[0], c1 = bhi + pcs[1], c2 = bhi + pcs[2], c3 = bhi + pcs[3];
;                   asm volatile("ds_read_b64_tr_b16 %0, %8\n\tds_read_b64_tr_b16 %1, %9\n\tds_read_b64_tr_b16 %2, %10\n\tds_read_b64_tr_b16 %3, %11\n\t"
;                                "ds_read_b64_tr_b16 %4, %12\n\tds_read_b64_tr_b16 %5, %13\n\tds_read_b64_tr_b16 %6, %14\n\tds_read_b64_tr_b16 %7, %15\n\ts_waitcnt lgkmcnt(0)"
;                                : "=&v"(l0), "=&v"(l1), "=&v"(l2), "=&v"(l3), "=&v"(h0), "=&v"(h1), "=&v"(h2), "=&v"(h3) : "v"(a0), "v"(a1), "v"(a2), "v"(a3), "v"(c0), "v"(c1), "v"(c2), "v"(c3) : "memory"); }
;               else asm volatile("ds_read_b64_tr_b16 %0, %4\n\tds_read_b64_tr_b16 %1, %5\n\tds_read_b64_tr_b16 %2, %6\n\tds_read_b64_tr_b16 %3, %7\n\ts_waitcnt lgkmcnt(0)"
;                                 : "=&v"(l0), "=&v"(l1), "=&v"(l2), "=&v"(l3) : "v"(a0), "v"(a1), "v"(a2), "v"(a3) : "memory");
;               const bf16x8s pf = __builtin_bit_cast(bf16x8s, pb[t]);
;               O[0] = __builtin_amdgcn_mfma_f32_16x16x32_bf16(__builtin_bit_cast(bf16x8s, ((v4u){l0.x, l0.y, h0.x, h0.y})), pf, O[0], 0, 0, 0);
	v_add_u32_e32 v31, s1, v82
	v_add_u32_e32 v85, s1, v81
	v_add_u32_e32 v98, s1, v80
	v_add_u32_e32 v99, s1, v79
	s_add_i32 s1, s83, s87
	s_add_i32 s1, s1, s0
	s_lshl_b32 s1, s1, 15
	s_and_b32 s1, s1, 0x18000
	s_add_i32 s1, s97, s1
	s_addk_i32 s1, 0x4000
	v_add_u32_e32 v100, s1, v79
	v_add_u32_e32 v101, s1, v80
	v_add_u32_e32 v102, s1, v81
	v_add_u32_e32 v103, s1, v82
	s_add_i32 s1, s84, s87
	s_add_i32 s1, s1, s0
	v_mfma_f32_16x16x32_bf16 v[44:47], v[44:47], v[24:27], 0
	s_lshl_b32 s1, s1, 15
	s_and_b32 s1, s1, 0x18000
	s_add_i32 s1, s58, s1
	v_mfma_f32_16x16x32_bf16 v[40:43], v[40:43], v[24:27], 0
	s_addk_i32 s1, 0x4000
	v_mov_b32_e32 v2, v3
	v_mov_b32_e32 v30, v29
	s_nop 1
	v_permlane16_swap_b32_e32 v30, v29
	v_mfma_f32_16x16x32_bf16 v[36:39], v[36:39], v[24:27], 0
	s_waitcnt lgkmcnt(0)
	v_add_f32_e32 v29, v29, v30
	v_mfma_f32_16x16x32_bf16 v[24:27], v[32:35], v[24:27], 0
	ds_read_b64_tr_b16 v[94:95], v99
	ds_read_b64_tr_b16 v[90:91], v98
	ds_read_b64_tr_b16 v[86:87], v85
	ds_read_b64_tr_b16 v[32:33], v31
	ds_read_b64_tr_b16 v[96:97], v100
	ds_read_b64_tr_b16 v[92:93], v101
	ds_read_b64_tr_b16 v[88:89], v102
	ds_read_b64_tr_b16 v[34:35], v103
	s_waitcnt lgkmcnt(0)
	v_add_u32_e32 v31, s1, v82
	v_add_u32_e32 v85, s1, v81
	v_mfma_f32_16x16x32_bf16 v[44:47], v[94:97], v[20:23], v[44:47]
	v_add_u32_e32 v94, s1, v80
	v_add_u32_e32 v95, s1, v79
	s_add_i32 s1, s85, s87
	s_add_i32 s1, s1, s0
	s_lshl_b32 s1, s1, 15
	s_and_b32 s1, s1, 0x18000
	s_add_i32 s1, s59, s1
	s_addk_i32 s1, 0x4000
	v_add_u32_e32 v96, s1, v79
	v_add_u32_e32 v97, s1, v80
	v_add_u32_e32 v98, s1, v81
	v_add_u32_e32 v99, s1, v82
	s_add_i32 s1, s86, s87
	s_add_i32 s1, s1, s0
	s_lshl_b32 s1, s1, 15
	s_and_b32 s1, s1, 0x18000
	s_add_i32 s1, s38, s1
	v_mfma_f32_16x16x32_bf16 v[40:43], v[90:93], v[20:23], v[40:43]
	s_addk_i32 s1, 0x4000
	v_mov_b32_e32 v30, v29
	s_nop 1
	v_permlane32_swap_b32_e32 v30, v29
	v_mfma_f32_16x16x32_bf16 v[36:39], v[86:89], v[20:23], v[36:39]
	v_mfma_f32_16x16x32_bf16 v[20:23], v[32:35], v[20:23], v[24:27]
	ds_read_b64_tr_b16 v[90:91], v95
	ds_read_b64_tr_b16 v[86:87], v94
	ds_read_b64_tr_b16 v[32:33], v85
	ds_read_b64_tr_b16 v[24:25], v31
	ds_read_b64_tr_b16 v[92:93], v96
	ds_read_b64_tr_b16 v[88:89], v97
	ds_read_b64_tr_b16 v[34:35], v98
	ds_read_b64_tr_b16 v[26:27], v99
	s_waitcnt lgkmcnt(0)
	v_add_u32_e32 v31, s1, v82
	v_add_u32_e32 v85, s1, v81
	v_mfma_f32_16x16x32_bf16 v[44:47], v[90:93], v[16:19], v[44:47]
	v_add_u32_e32 v90, s1, v80
	v_add_u32_e32 v91, s1, v79
	s_add_i32 s1, s89, s87
	s_add_i32 s1, s1, s0
	s_lshl_b32 s1, s1, 15
	s_and_b32 s1, s1, 0x18000
	s_add_i32 s1, s40, s1
	s_addk_i32 s1, 0x4000
	v_add_u32_e32 v92, s1, v79
	v_add_u32_e32 v93, s1, v80
	v_add_u32_e32 v94, s1, v81
	v_add_u32_e32 v95, s1, v82
	s_add_i32 s1, s91, s87
	s_add_i32 s1, s1, s0
	v_mfma_f32_16x16x32_bf16 v[40:43], v[86:89], v[16:19], v[40:43]
	s_lshl_b32 s0, s1, 15
	s_and_b32 s0, s0, 0x18000
	s_add_i32 s0, s93, s0
	v_mfma_f32_16x16x32_bf16 v[32:35], v[32:35], v[16:19], v[36:39]
	s_addk_i32 s0, 0x4000
	v_mfma_f32_16x16x32_bf16 v[16:19], v[24:27], v[16:19], v[20:23]
	ds_read_b64_tr_b16 v[86:87], v91
	ds_read_b64_tr_b16 v[36:37], v90
	ds_read_b64_tr_b16 v[24:25], v85
	ds_read_b64_tr_b16 v[20:21], v31
	ds_read_b64_tr_b16 v[88:89], v92
	ds_read_b64_tr_b16 v[38:39], v93
	ds_read_b64_tr_b16 v[26:27], v94
	ds_read_b64_tr_b16 v[22:23], v95
	s_waitcnt lgkmcnt(0)
	s_nop 0
	v_mfma_f32_16x16x32_bf16 v[44:47], v[86:89], v[12:15], v[44:47]
	v_mfma_f32_16x16x32_bf16 v[36:39], v[36:39], v[12:15], v[40:43]
	v_mfma_f32_16x16x32_bf16 v[32:35], v[24:27], v[12:15], v[32:35]
	v_add_u32_e32 v24, s0, v80
	v_add_u32_e32 v25, s0, v79
	v_mov_b32_e32 v42, v3
	v_mfma_f32_16x16x32_bf16 v[12:15], v[20:23], v[12:15], v[16:19]
	v_add_u32_e32 v22, s0, v82
	v_add_u32_e32 v23, s0, v81
	ds_read_b64_tr_b16 v[20:21], v25
	ds_read_b64_tr_b16 v[18:19], v24
	ds_read_b64_tr_b16 v[16:17], v23
	ds_read_b64_tr_b16 v[40:41], v22
	s_waitcnt lgkmcnt(0)
	v_mov_b32_e32 v22, v3
	v_mov_b32_e32 v23, v3
	v_mov_b32_e32 v43, v3
	s_nop 0
	v_mfma_f32_16x16x32_bf16 v[24:27], v[20:23], v[0:3], v[44:47]
	v_mov_b32_e32 v20, v3
	v_mov_b32_e32 v21, v3
	v_mfma_f32_16x16x32_bf16 v[12:15], v[40:43], v[0:3], v[12:15]
	s_nop 0
	v_mfma_f32_16x16x32_bf16 v[20:23], v[18:21], v[0:3], v[36:39]
	v_mov_b32_e32 v18, v3
	v_mov_b32_e32 v19, v3
	s_nop 1
	v_mfma_f32_16x16x32_bf16 v[16:19], v[16:19], v[0:3], v[32:35]
	s_waitcnt lgkmcnt(0)
	v_add_f32_e32 v1, v29, v30
	v_rcp_f32_e32 v0, v1
	v_log_f32_e32 v1, v1
	v_mov_b32_e32 v2, 0
	v_add_f32_e32 v28, v28, v1
	s_cbranch_vccnz .LBB0_245
	v_max_f32_e32 v1, v28, v28
	s_waitcnt vmcnt(0)
	v_max_f32_e32 v2, v84, v84
	v_max_f32_e32 v2, v2, v1
	v_sub_f32_e32 v1, v84, v2
	v_sub_f32_e32 v28, v28, v2
	v_exp_f32_e32 v1, v1
	v_exp_f32_e32 v28, v28
	s_nop 0
	v_add_f32_e32 v30, v1, v28
	v_rcp_f32_e32 v29, v30
	v_log_f32_e32 v30, v30
	v_mul_f32_e32 v28, v28, v29
	v_pk_mul_f32 v[0:1], v[0:1], v[28:29]
	v_add_f32_e32 v28, v2, v30
	v_mov_b32_e32 v2, v1
